# attention epilogues (DSA and FoX): the xor-1 lane exchange done with a DPP quad_perm move instead of ds_bpermute_b32 (no LDS round trip per output element)
# speedup vs baseline: 1.0107x; 1.0002x over previous
; __device__ __forceinline__ unsigned cvt_pk_bf16(float lo, float hi) { unsigned r; asm volatile("v_cvt_pk_bf16_f32 %0, %1, %2" : "=v"(r) : "v"(lo), "v"(hi)); return r; }
; __device__ __forceinline__ float bf_lo(unsigned w) { return __uint_as_float(w << 16); }
; __device__ __forceinline__ float bf_hi(unsigned w) { return __uint_as_float(w & 0xffff0000u); }
; __device__ __forceinline__ int crow(int r, int hi) { return (r & 3) + 8 * (r >> 2) + 4 * hi; }
; template <int MODE> ...
;     ...
;     if (part) {
;         if (hi == 0) { pml[(wid * QBLK + r32) * 2] = m_reg; pml[(wid * QBLK + r32) * 2 + 1] = l_reg; }
; #pragma unroll
;         for (int r = 0; r < 16; ++r)
; #pragma unroll
;             for (int d0 = 0; d0 < 4; ++d0) part[(size_t)(wid * QBLK + crow(r, hi)) * D + d0 * 32 + r32] = o[d0][r];
;         return;
;     }
;     if (hi == 0) li_l[r32] = l_reg; asm volatile("s_waitcnt lgkmcnt(0)" ::: "memory");
; #pragma unroll
;     for (int r = 0; r < 16; ++r) { const int orow = qlo + crow(r, hi); const float rl = __builtin_amdgcn_rcpf(li_l[crow(r, hi)]);
; #pragma unroll
;         for (int d0 = 0; d0 < 4; ++d0) { float v = o[d0][r] * rl; float vn = __shfl_xor(v, 1);
;             if ((r32 & 1) == 0) { const int col = d0 * 32 + r32;
;                 if (MODE == 1) { const unsigned g = *(const unsigned*)(gate + (size_t)orow * 1024 + hoff + col); v *= bf_lo(g); vn *= bf_hi(g); }
;                 *(unsigned*)(Ob + (size_t)orow * DM + ocol0 + col) = cvt_pk_bf16(v, vn); } } }
.LBB0_1227:
	s_lshl_b64 s[0:1], 1, s10
	s_and_b32 s1, s1, 0xff08
	s_and_b32 s0, s0, 0x42108421
	s_cmp_lg_u64 s[0:1], 0
	v_cmp_gt_u32_e64 s[2:3], 32, v192
	s_cbranch_scc0 .LBB0_1359
	s_and_saveexec_b64 s[0:1], s[2:3]
	v_lshl_add_u32 v66, v190, 2, s62
	ds_write_b32 v66, v181
	s_or_b64 exec, exec, s[0:1]
	s_waitcnt lgkmcnt(0)
	v_lshl_add_u32 v71, v191, 4, s62
	ds_read_b32 v68, v71
	v_and_b32_e32 v67, 64, v1
	v_xor_b32_e32 v66, 1, v1
	v_add_u32_e32 v67, 64, v67
	v_cmp_lt_i32_e32 vcc, v66, v67
	s_waitcnt lgkmcnt(0)
	v_rcp_f32_e32 v72, v68
	v_lshlrev_b32_e32 v178, 1, v190
	v_cndmask_b32_e32 v66, v1, v66, vcc
	v_lshlrev_b32_e32 v70, 2, v66
	v_mul_f32_e32 v73, v2, v72
	v_and_b32_e32 v66, 1, v192
	s_nop 1
	v_mov_b32_dpp v74, v73 quad_perm:[1,0,3,2] row_mask:0xf bank_mask:0xf
	v_cmp_eq_u32_e32 vcc, 0, v66
	v_add_u32_e32 v66, s59, v193
	v_ashrrev_i32_e32 v67, 31, v66
	v_lshlrev_b64 v[68:69], 12, v[66:67]
	v_lshl_add_u64 v[68:69], s[22:23], 0, v[68:69]
	s_and_saveexec_b64 s[0:1], vcc
	s_cbranch_execz .LBB0_1232
	v_lshl_add_u64 v[76:77], v[68:69], 0, v[178:179]
	s_waitcnt lgkmcnt(0)
	v_cvt_pk_bf16_f32 v67, v73, v74
	global_store_dword v[76:77], v67, off
.LBB0_1232:
	s_or_b64 exec, exec, s[0:1]
	v_mul_f32_e32 v67, v50, v72
	s_nop 1
	v_mov_b32_dpp v73, v67 quad_perm:[1,0,3,2] row_mask:0xf bank_mask:0xf
	s_and_saveexec_b64 s[0:1], vcc
	s_cbranch_execz .LBB0_1234
	s_waitcnt lgkmcnt(0)
	v_lshl_add_u64 v[74:75], v[68:69], 0, v[178:179]
	s_waitcnt lgkmcnt(0)
	v_cvt_pk_bf16_f32 v67, v67, v73
	global_store_dword v[74:75], v67, off offset:64
.LBB0_1234:
	s_or_b64 exec, exec, s[0:1]
	v_mul_f32_e32 v67, v34, v72
	s_waitcnt lgkmcnt(0)
	s_nop 1
	v_mov_b32_dpp v73, v67 quad_perm:[1,0,3,2] row_mask:0xf bank_mask:0xf
	s_and_saveexec_b64 s[0:1], vcc
	s_cbranch_execz .LBB0_1236
	v_lshl_add_u64 v[74:75], v[68:69], 0, v[178:179]
	s_waitcnt lgkmcnt(0)
	v_cvt_pk_bf16_f32 v67, v67, v73
	global_store_dword v[74:75], v67, off offset:128
.LBB0_1236:
	s_or_b64 exec, exec, s[0:1]
	v_mul_f32_e32 v67, v18, v72
	s_nop 1
	v_mov_b32_dpp v72, v67 quad_perm:[1,0,3,2] row_mask:0xf bank_mask:0xf
	s_and_saveexec_b64 s[0:1], vcc
	s_cbranch_execz .LBB0_1238
	v_lshl_add_u64 v[68:69], v[68:69], 0, v[178:179]
	s_waitcnt lgkmcnt(0)
	v_cvt_pk_bf16_f32 v67, v67, v72
	global_store_dword v[68:69], v67, off offset:192
.LBB0_1238:
	s_or_b64 exec, exec, s[0:1]
	ds_read_b32 v67, v71 offset:4
	v_add3_u32 v68, s59, v193, 1
	v_ashrrev_i32_e32 v69, 31, v68
	v_lshlrev_b64 v[68:69], 12, v[68:69]
	v_lshl_add_u64 v[68:69], s[22:23], 0, v[68:69]
	s_waitcnt lgkmcnt(0)
	v_rcp_f32_e32 v67, v67
	s_nop 0
	v_mul_f32_e32 v72, v3, v67
	s_nop 1
	v_mov_b32_dpp v73, v72 quad_perm:[1,0,3,2] row_mask:0xf bank_mask:0xf
	s_and_saveexec_b64 s[0:1], vcc
	s_cbranch_execz .LBB0_1240
	v_lshl_add_u64 v[74:75], v[68:69], 0, v[178:179]
	s_waitcnt lgkmcnt(0)
	v_cvt_pk_bf16_f32 v72, v72, v73
	global_store_dword v[74:75], v72, off
.LBB0_1240:
	s_or_b64 exec, exec, s[0:1]
	v_mul_f32_e32 v72, v51, v67
	s_waitcnt lgkmcnt(0)
	s_nop 1
	v_mov_b32_dpp v73, v72 quad_perm:[1,0,3,2] row_mask:0xf bank_mask:0xf
	s_and_saveexec_b64 s[0:1], vcc
	s_cbranch_execz .LBB0_1242
	v_lshl_add_u64 v[74:75], v[68:69], 0, v[178:179]
	s_waitcnt lgkmcnt(0)
	v_cvt_pk_bf16_f32 v72, v72, v73
	global_store_dword v[74:75], v72, off offset:64
.LBB0_1242:
	s_or_b64 exec, exec, s[0:1]
	v_mul_f32_e32 v72, v35, v67
	s_waitcnt lgkmcnt(0)
	s_nop 1
	v_mov_b32_dpp v73, v72 quad_perm:[1,0,3,2] row_mask:0xf bank_mask:0xf
	s_and_saveexec_b64 s[0:1], vcc
	s_cbranch_execz .LBB0_1244
	v_lshl_add_u64 v[74:75], v[68:69], 0, v[178:179]
	s_waitcnt lgkmcnt(0)
	v_cvt_pk_bf16_f32 v72, v72, v73
	global_store_dword v[74:75], v72, off offset:128
.LBB0_1244:
	s_or_b64 exec, exec, s[0:1]
	v_mul_f32_e32 v67, v19, v67
	s_nop 1
	v_mov_b32_dpp v72, v67 quad_perm:[1,0,3,2] row_mask:0xf bank_mask:0xf
	s_and_saveexec_b64 s[0:1], vcc
	s_cbranch_execz .LBB0_1246
	v_lshl_add_u64 v[68:69], v[68:69], 0, v[178:179]
	s_waitcnt lgkmcnt(0)
	v_cvt_pk_bf16_f32 v67, v67, v72
	global_store_dword v[68:69], v67, off offset:192
.LBB0_1246:
	s_or_b64 exec, exec, s[0:1]
	ds_read_b32 v67, v71 offset:8
	v_add3_u32 v68, s59, v193, 2
	v_ashrrev_i32_e32 v69, 31, v68
	v_lshlrev_b64 v[68:69], 12, v[68:69]
	v_lshl_add_u64 v[68:69], s[22:23], 0, v[68:69]
	s_waitcnt lgkmcnt(0)
	v_rcp_f32_e32 v67, v67
	s_nop 0
	v_mul_f32_e32 v72, v4, v67
	s_nop 1
	v_mov_b32_dpp v73, v72 quad_perm:[1,0,3,2] row_mask:0xf bank_mask:0xf
	s_and_saveexec_b64 s[0:1], vcc
	s_cbranch_execz .LBB0_1248
	v_lshl_add_u64 v[74:75], v[68:69], 0, v[178:179]
	s_waitcnt lgkmcnt(0)
	v_cvt_pk_bf16_f32 v72, v72, v73
	global_store_dword v[74:75], v72, off
.LBB0_1248:
	s_or_b64 exec, exec, s[0:1]
	v_mul_f32_e32 v72, v52, v67
	s_waitcnt lgkmcnt(0)
	s_nop 1
	v_mov_b32_dpp v73, v72 quad_perm:[1,0,3,2] row_mask:0xf bank_mask:0xf
	s_and_saveexec_b64 s[0:1], vcc
	s_cbranch_execz .LBB0_1250
	v_lshl_add_u64 v[74:75], v[68:69], 0, v[178:179]
	s_waitcnt lgkmcnt(0)
	v_cvt_pk_bf16_f32 v72, v72, v73
	global_store_dword v[74:75], v72, off offset:64
.LBB0_1250:
	s_or_b64 exec, exec, s[0:1]
	v_mul_f32_e32 v72, v36, v67
	s_waitcnt lgkmcnt(0)
	s_nop 1
	v_mov_b32_dpp v73, v72 quad_perm:[1,0,3,2] row_mask:0xf bank_mask:0xf
	s_and_saveexec_b64 s[0:1], vcc
	s_cbranch_execz .LBB0_1252
	v_lshl_add_u64 v[74:75], v[68:69], 0, v[178:179]
	s_waitcnt lgkmcnt(0)
	v_cvt_pk_bf16_f32 v72, v72, v73
	global_store_dword v[74:75], v72, off offset:128
.LBB0_1252:
	s_or_b64 exec, exec, s[0:1]
	v_mul_f32_e32 v67, v20, v67
	s_nop 1
	v_mov_b32_dpp v72, v67 quad_perm:[1,0,3,2] row_mask:0xf bank_mask:0xf
	s_and_saveexec_b64 s[0:1], vcc
	s_cbranch_execz .LBB0_1254
	v_lshl_add_u64 v[68:69], v[68:69], 0, v[178:179]
	s_waitcnt lgkmcnt(0)
	v_cvt_pk_bf16_f32 v67, v67, v72
	global_store_dword v[68:69], v67, off offset:192
; __device__ __forceinline__ unsigned cvt_pk_bf16(float lo, float hi) { unsigned r; asm volatile("v_cvt_pk_bf16_f32 %0, %1, %2" : "=v"(r) : "v"(lo), "v"(hi)); return r; }
; __device__ __forceinline__ float bf_lo(unsigned w) { return __uint_as_float(w << 16); }
; __device__ __forceinline__ float bf_hi(unsigned w) { return __uint_as_float(w & 0xffff0000u); }
; __device__ __forceinline__ int crow(int r, int hi) { return (r & 3) + 8 * (r >> 2) + 4 * hi; }
; template <int MODE> ...
;     ...
;     if (hi == 0) li_l[r32] = l_reg; asm volatile("s_waitcnt lgkmcnt(0)" ::: "memory");
; #pragma unroll
;     for (int r = 0; r < 16; ++r) { const int orow = qlo + crow(r, hi); const float rl = __builtin_amdgcn_rcpf(li_l[crow(r, hi)]);
; #pragma unroll
;         for (int d0 = 0; d0 < 4; ++d0) { float v = o[d0][r] * rl; float vn = __shfl_xor(v, 1);
;             if ((r32 & 1) == 0) { const int col = d0 * 32 + r32;
;                 if (MODE == 1) { const unsigned g = *(const unsigned*)(gate + (size_t)orow * 1024 + hoff + col); v *= bf_lo(g); vn *= bf_hi(g); }
;                 *(unsigned*)(Ob + (size_t)orow * DM + ocol0 + col) = cvt_pk_bf16(v, vn); } } }
.LBB0_1254:
	s_or_b64 exec, exec, s[0:1]
	ds_read_b32 v67, v71 offset:12
	v_add3_u32 v68, s59, v193, 3
	v_ashrrev_i32_e32 v69, 31, v68
	v_lshlrev_b64 v[68:69], 12, v[68:69]
	v_lshl_add_u64 v[68:69], s[22:23], 0, v[68:69]
	s_waitcnt lgkmcnt(0)
	v_rcp_f32_e32 v67, v67
	s_nop 0
	v_mul_f32_e32 v72, v5, v67
	s_nop 1
	v_mov_b32_dpp v73, v72 quad_perm:[1,0,3,2] row_mask:0xf bank_mask:0xf
	s_and_saveexec_b64 s[0:1], vcc
	s_cbranch_execz .LBB0_1256
	v_lshl_add_u64 v[74:75], v[68:69], 0, v[178:179]
	s_waitcnt lgkmcnt(0)
	v_cvt_pk_bf16_f32 v72, v72, v73
	global_store_dword v[74:75], v72, off
.LBB0_1256:
	s_or_b64 exec, exec, s[0:1]
	v_mul_f32_e32 v72, v53, v67
	s_waitcnt lgkmcnt(0)
	s_nop 1
	v_mov_b32_dpp v73, v72 quad_perm:[1,0,3,2] row_mask:0xf bank_mask:0xf
	s_and_saveexec_b64 s[0:1], vcc
	s_cbranch_execz .LBB0_1258
	v_lshl_add_u64 v[74:75], v[68:69], 0, v[178:179]
	s_waitcnt lgkmcnt(0)
	v_cvt_pk_bf16_f32 v72, v72, v73
	global_store_dword v[74:75], v72, off offset:64
.LBB0_1258:
	s_or_b64 exec, exec, s[0:1]
	v_mul_f32_e32 v72, v37, v67
	s_waitcnt lgkmcnt(0)
	s_nop 1
	v_mov_b32_dpp v73, v72 quad_perm:[1,0,3,2] row_mask:0xf bank_mask:0xf
	s_and_saveexec_b64 s[0:1], vcc
	s_cbranch_execz .LBB0_1260
	v_lshl_add_u64 v[74:75], v[68:69], 0, v[178:179]
	s_waitcnt lgkmcnt(0)
	v_cvt_pk_bf16_f32 v72, v72, v73
	global_store_dword v[74:75], v72, off offset:128
.LBB0_1260:
	s_or_b64 exec, exec, s[0:1]
	v_mul_f32_e32 v67, v21, v67
	s_nop 1
	v_mov_b32_dpp v72, v67 quad_perm:[1,0,3,2] row_mask:0xf bank_mask:0xf
	s_and_saveexec_b64 s[0:1], vcc
	s_cbranch_execz .LBB0_1262
	v_lshl_add_u64 v[68:69], v[68:69], 0, v[178:179]
	s_waitcnt lgkmcnt(0)
	v_cvt_pk_bf16_f32 v67, v67, v72
	global_store_dword v[68:69], v67, off offset:192
.LBB0_1262:
	s_or_b64 exec, exec, s[0:1]
	ds_read_b32 v67, v71 offset:32
	v_add_u32_e32 v68, 8, v66
	v_ashrrev_i32_e32 v69, 31, v68
	v_lshlrev_b64 v[68:69], 12, v[68:69]
	v_lshl_add_u64 v[68:69], s[22:23], 0, v[68:69]
	s_waitcnt lgkmcnt(0)
	v_rcp_f32_e32 v67, v67
	s_nop 0
	v_mul_f32_e32 v72, v6, v67
	s_nop 1
	v_mov_b32_dpp v73, v72 quad_perm:[1,0,3,2] row_mask:0xf bank_mask:0xf
	s_and_saveexec_b64 s[0:1], vcc
	s_cbranch_execz .LBB0_1264
	v_lshl_add_u64 v[74:75], v[68:69], 0, v[178:179]
	s_waitcnt lgkmcnt(0)
	v_cvt_pk_bf16_f32 v72, v72, v73
	global_store_dword v[74:75], v72, off
.LBB0_1264:
	s_or_b64 exec, exec, s[0:1]
	v_mul_f32_e32 v72, v54, v67
	s_waitcnt lgkmcnt(0)
	s_nop 1
	v_mov_b32_dpp v73, v72 quad_perm:[1,0,3,2] row_mask:0xf bank_mask:0xf
	s_and_saveexec_b64 s[0:1], vcc
	s_cbranch_execz .LBB0_1266
	v_lshl_add_u64 v[74:75], v[68:69], 0, v[178:179]
	s_waitcnt lgkmcnt(0)
	v_cvt_pk_bf16_f32 v72, v72, v73
	global_store_dword v[74:75], v72, off offset:64
.LBB0_1266:
	s_or_b64 exec, exec, s[0:1]
	v_mul_f32_e32 v72, v38, v67
	s_waitcnt lgkmcnt(0)
	s_nop 1
	v_mov_b32_dpp v73, v72 quad_perm:[1,0,3,2] row_mask:0xf bank_mask:0xf
	s_and_saveexec_b64 s[0:1], vcc
	s_cbranch_execz .LBB0_1268
	v_lshl_add_u64 v[74:75], v[68:69], 0, v[178:179]
	s_waitcnt lgkmcnt(0)
	v_cvt_pk_bf16_f32 v72, v72, v73
	global_store_dword v[74:75], v72, off offset:128
.LBB0_1268:
	s_or_b64 exec, exec, s[0:1]
	v_mul_f32_e32 v67, v22, v67
	s_nop 1
	v_mov_b32_dpp v72, v67 quad_perm:[1,0,3,2] row_mask:0xf bank_mask:0xf
	s_and_saveexec_b64 s[0:1], vcc
	s_cbranch_execz .LBB0_1270
	v_lshl_add_u64 v[68:69], v[68:69], 0, v[178:179]
	s_waitcnt lgkmcnt(0)
	v_cvt_pk_bf16_f32 v67, v67, v72
	global_store_dword v[68:69], v67, off offset:192
.LBB0_1270:
	s_or_b64 exec, exec, s[0:1]
	ds_read_b32 v67, v71 offset:36
	v_add_u32_e32 v68, 9, v66
	v_ashrrev_i32_e32 v69, 31, v68
	v_lshlrev_b64 v[68:69], 12, v[68:69]
	v_lshl_add_u64 v[68:69], s[22:23], 0, v[68:69]
	s_waitcnt lgkmcnt(0)
	v_rcp_f32_e32 v67, v67
	s_nop 0
	v_mul_f32_e32 v72, v7, v67
	s_nop 1
	v_mov_b32_dpp v73, v72 quad_perm:[1,0,3,2] row_mask:0xf bank_mask:0xf
	s_and_saveexec_b64 s[0:1], vcc
	s_cbranch_execz .LBB0_1272
	v_lshl_add_u64 v[74:75], v[68:69], 0, v[178:179]
	s_waitcnt lgkmcnt(0)
	v_cvt_pk_bf16_f32 v72, v72, v73
	global_store_dword v[74:75], v72, off
.LBB0_1272:
	s_or_b64 exec, exec, s[0:1]
	v_mul_f32_e32 v72, v55, v67
	s_waitcnt lgkmcnt(0)
	s_nop 1
	v_mov_b32_dpp v73, v72 quad_perm:[1,0,3,2] row_mask:0xf bank_mask:0xf
	s_and_saveexec_b64 s[0:1], vcc
	s_cbranch_execz .LBB0_1274
	v_lshl_add_u64 v[74:75], v[68:69], 0, v[178:179]
	s_waitcnt lgkmcnt(0)
	v_cvt_pk_bf16_f32 v72, v72, v73
	global_store_dword v[74:75], v72, off offset:64
.LBB0_1274:
	s_or_b64 exec, exec, s[0:1]
	v_mul_f32_e32 v72, v39, v67
	s_waitcnt lgkmcnt(0)
	s_nop 1
	v_mov_b32_dpp v73, v72 quad_perm:[1,0,3,2] row_mask:0xf bank_mask:0xf
	s_and_saveexec_b64 s[0:1], vcc
	s_cbranch_execz .LBB0_1276
	v_lshl_add_u64 v[74:75], v[68:69], 0, v[178:179]
	s_waitcnt lgkmcnt(0)
	v_cvt_pk_bf16_f32 v72, v72, v73
	global_store_dword v[74:75], v72, off offset:128
.LBB0_1276:
	s_or_b64 exec, exec, s[0:1]
	v_mul_f32_e32 v67, v23, v67
	s_nop 1
	v_mov_b32_dpp v72, v67 quad_perm:[1,0,3,2] row_mask:0xf bank_mask:0xf
	s_and_saveexec_b64 s[0:1], vcc
	s_cbranch_execz .LBB0_1278
	v_lshl_add_u64 v[68:69], v[68:69], 0, v[178:179]
	s_waitcnt lgkmcnt(0)
	v_cvt_pk_bf16_f32 v67, v67, v72
	global_store_dword v[68:69], v67, off offset:192
.LBB0_1278:
	s_or_b64 exec, exec, s[0:1]
	ds_read_b32 v67, v71 offset:40
	v_add_u32_e32 v68, 10, v66
	v_ashrrev_i32_e32 v69, 31, v68
	v_lshlrev_b64 v[68:69], 12, v[68:69]
	v_lshl_add_u64 v[68:69], s[22:23], 0, v[68:69]
	s_waitcnt lgkmcnt(0)
	v_rcp_f32_e32 v67, v67
	s_nop 0
	v_mul_f32_e32 v72, v8, v67
	s_nop 1
	v_mov_b32_dpp v73, v72 quad_perm:[1,0,3,2] row_mask:0xf bank_mask:0xf
	s_and_saveexec_b64 s[0:1], vcc
	s_cbranch_execz .LBB0_1280
	v_lshl_add_u64 v[74:75], v[68:69], 0, v[178:179]
	s_waitcnt lgkmcnt(0)
	v_cvt_pk_bf16_f32 v72, v72, v73
	global_store_dword v[74:75], v72, off
; __device__ __forceinline__ unsigned cvt_pk_bf16(float lo, float hi) { unsigned r; asm volatile("v_cvt_pk_bf16_f32 %0, %1, %2" : "=v"(r) : "v"(lo), "v"(hi)); return r; }
; __device__ __forceinline__ float bf_lo(unsigned w) { return __uint_as_float(w << 16); }
; __device__ __forceinline__ float bf_hi(unsigned w) { return __uint_as_float(w & 0xffff0000u); }
; __device__ __forceinline__ int crow(int r, int hi) { return (r & 3) + 8 * (r >> 2) + 4 * hi; }
; template <int MODE> ...
;     ...
;     if (hi == 0) li_l[r32] = l_reg; asm volatile("s_waitcnt lgkmcnt(0)" ::: "memory");
; #pragma unroll
;     for (int r = 0; r < 16; ++r) { const int orow = qlo + crow(r, hi); const float rl = __builtin_amdgcn_rcpf(li_l[crow(r, hi)]);
; #pragma unroll
;         for (int d0 = 0; d0 < 4; ++d0) { float v = o[d0][r] * rl; float vn = __shfl_xor(v, 1);
;             if ((r32 & 1) == 0) { const int col = d0 * 32 + r32;
;                 if (MODE == 1) { const unsigned g = *(const unsigned*)(gate + (size_t)orow * 1024 + hoff + col); v *= bf_lo(g); vn *= bf_hi(g); }
;                 *(unsigned*)(Ob + (size_t)orow * DM + ocol0 + col) = cvt_pk_bf16(v, vn); } } }
.LBB0_1280:
	s_or_b64 exec, exec, s[0:1]
	v_mul_f32_e32 v72, v56, v67
	s_waitcnt lgkmcnt(0)
	s_nop 1
	v_mov_b32_dpp v73, v72 quad_perm:[1,0,3,2] row_mask:0xf bank_mask:0xf
	s_and_saveexec_b64 s[0:1], vcc
	s_cbranch_execz .LBB0_1282
	v_lshl_add_u64 v[74:75], v[68:69], 0, v[178:179]
	s_waitcnt lgkmcnt(0)
	v_cvt_pk_bf16_f32 v72, v72, v73
	global_store_dword v[74:75], v72, off offset:64
.LBB0_1282:
	s_or_b64 exec, exec, s[0:1]
	v_mul_f32_e32 v72, v40, v67
	s_waitcnt lgkmcnt(0)
	s_nop 1
	v_mov_b32_dpp v73, v72 quad_perm:[1,0,3,2] row_mask:0xf bank_mask:0xf
	s_and_saveexec_b64 s[0:1], vcc
	s_cbranch_execz .LBB0_1284
	v_lshl_add_u64 v[74:75], v[68:69], 0, v[178:179]
	s_waitcnt lgkmcnt(0)
	v_cvt_pk_bf16_f32 v72, v72, v73
	global_store_dword v[74:75], v72, off offset:128
.LBB0_1284:
	s_or_b64 exec, exec, s[0:1]
	v_mul_f32_e32 v67, v24, v67
	s_nop 1
	v_mov_b32_dpp v72, v67 quad_perm:[1,0,3,2] row_mask:0xf bank_mask:0xf
	s_and_saveexec_b64 s[0:1], vcc
	s_cbranch_execz .LBB0_1286
	v_lshl_add_u64 v[68:69], v[68:69], 0, v[178:179]
	s_waitcnt lgkmcnt(0)
	v_cvt_pk_bf16_f32 v67, v67, v72
	global_store_dword v[68:69], v67, off offset:192
.LBB0_1286:
	s_or_b64 exec, exec, s[0:1]
	ds_read_b32 v67, v71 offset:44
	v_add_u32_e32 v68, 11, v66
	v_ashrrev_i32_e32 v69, 31, v68
	v_lshlrev_b64 v[68:69], 12, v[68:69]
	v_lshl_add_u64 v[68:69], s[22:23], 0, v[68:69]
	s_waitcnt lgkmcnt(0)
	v_rcp_f32_e32 v67, v67
	s_nop 0
	v_mul_f32_e32 v72, v9, v67
	s_nop 1
	v_mov_b32_dpp v73, v72 quad_perm:[1,0,3,2] row_mask:0xf bank_mask:0xf
	s_and_saveexec_b64 s[0:1], vcc
	s_cbranch_execz .LBB0_1288
	v_lshl_add_u64 v[74:75], v[68:69], 0, v[178:179]
	s_waitcnt lgkmcnt(0)
	v_cvt_pk_bf16_f32 v72, v72, v73
	global_store_dword v[74:75], v72, off
.LBB0_1288:
	s_or_b64 exec, exec, s[0:1]
	v_mul_f32_e32 v72, v57, v67
	s_waitcnt lgkmcnt(0)
	s_nop 1
	v_mov_b32_dpp v73, v72 quad_perm:[1,0,3,2] row_mask:0xf bank_mask:0xf
	s_and_saveexec_b64 s[0:1], vcc
	s_cbranch_execz .LBB0_1290
	v_lshl_add_u64 v[74:75], v[68:69], 0, v[178:179]
	s_waitcnt lgkmcnt(0)
	v_cvt_pk_bf16_f32 v72, v72, v73
	global_store_dword v[74:75], v72, off offset:64
.LBB0_1290:
	s_or_b64 exec, exec, s[0:1]
	v_mul_f32_e32 v72, v41, v67
	s_waitcnt lgkmcnt(0)
	s_nop 1
	v_mov_b32_dpp v73, v72 quad_perm:[1,0,3,2] row_mask:0xf bank_mask:0xf
	s_and_saveexec_b64 s[0:1], vcc
	s_cbranch_execz .LBB0_1292
	v_lshl_add_u64 v[74:75], v[68:69], 0, v[178:179]
	s_waitcnt lgkmcnt(0)
	v_cvt_pk_bf16_f32 v72, v72, v73
	global_store_dword v[74:75], v72, off offset:128
.LBB0_1292:
	s_or_b64 exec, exec, s[0:1]
	v_mul_f32_e32 v67, v25, v67
	s_nop 1
	v_mov_b32_dpp v72, v67 quad_perm:[1,0,3,2] row_mask:0xf bank_mask:0xf
	s_and_saveexec_b64 s[0:1], vcc
	s_cbranch_execz .LBB0_1294
	v_lshl_add_u64 v[68:69], v[68:69], 0, v[178:179]
	s_waitcnt lgkmcnt(0)
	v_cvt_pk_bf16_f32 v67, v67, v72
	global_store_dword v[68:69], v67, off offset:192
.LBB0_1294:
	s_or_b64 exec, exec, s[0:1]
	ds_read_b32 v67, v71 offset:64
	v_add_u32_e32 v68, 16, v66
	v_ashrrev_i32_e32 v69, 31, v68
	v_lshlrev_b64 v[68:69], 12, v[68:69]
	v_lshl_add_u64 v[68:69], s[22:23], 0, v[68:69]
	s_waitcnt lgkmcnt(0)
	v_rcp_f32_e32 v67, v67
	s_nop 0
	v_mul_f32_e32 v72, v10, v67
	s_nop 1
	v_mov_b32_dpp v73, v72 quad_perm:[1,0,3,2] row_mask:0xf bank_mask:0xf
	s_and_saveexec_b64 s[0:1], vcc
	s_cbranch_execz .LBB0_1296
	v_lshl_add_u64 v[74:75], v[68:69], 0, v[178:179]
	s_waitcnt lgkmcnt(0)
	v_cvt_pk_bf16_f32 v72, v72, v73
	global_store_dword v[74:75], v72, off
.LBB0_1296:
	s_or_b64 exec, exec, s[0:1]
	v_mul_f32_e32 v72, v58, v67
	s_waitcnt lgkmcnt(0)
	s_nop 1
	v_mov_b32_dpp v73, v72 quad_perm:[1,0,3,2] row_mask:0xf bank_mask:0xf
	s_and_saveexec_b64 s[0:1], vcc
	s_cbranch_execz .LBB0_1298
	v_lshl_add_u64 v[74:75], v[68:69], 0, v[178:179]
	s_waitcnt lgkmcnt(0)
	v_cvt_pk_bf16_f32 v72, v72, v73
	global_store_dword v[74:75], v72, off offset:64
.LBB0_1298:
	s_or_b64 exec, exec, s[0:1]
	v_mul_f32_e32 v72, v42, v67
	s_waitcnt lgkmcnt(0)
	s_nop 1
	v_mov_b32_dpp v73, v72 quad_perm:[1,0,3,2] row_mask:0xf bank_mask:0xf
	s_and_saveexec_b64 s[0:1], vcc
	s_cbranch_execz .LBB0_1300
	v_lshl_add_u64 v[74:75], v[68:69], 0, v[178:179]
	s_waitcnt lgkmcnt(0)
	v_cvt_pk_bf16_f32 v72, v72, v73
	global_store_dword v[74:75], v72, off offset:128
.LBB0_1300:
	s_or_b64 exec, exec, s[0:1]
	v_mul_f32_e32 v67, v26, v67
	s_nop 1
	v_mov_b32_dpp v72, v67 quad_perm:[1,0,3,2] row_mask:0xf bank_mask:0xf
	s_and_saveexec_b64 s[0:1], vcc
	s_cbranch_execz .LBB0_1302
	v_lshl_add_u64 v[68:69], v[68:69], 0, v[178:179]
	s_waitcnt lgkmcnt(0)
	v_cvt_pk_bf16_f32 v67, v67, v72
	global_store_dword v[68:69], v67, off offset:192
.LBB0_1302:
	s_or_b64 exec, exec, s[0:1]
	ds_read_b32 v67, v71 offset:68
	v_add_u32_e32 v68, 17, v66
	v_ashrrev_i32_e32 v69, 31, v68
	v_lshlrev_b64 v[68:69], 12, v[68:69]
	v_lshl_add_u64 v[68:69], s[22:23], 0, v[68:69]
	s_waitcnt lgkmcnt(0)
	v_rcp_f32_e32 v67, v67
	s_nop 0
	v_mul_f32_e32 v72, v11, v67
	s_nop 1
	v_mov_b32_dpp v73, v72 quad_perm:[1,0,3,2] row_mask:0xf bank_mask:0xf
	s_and_saveexec_b64 s[0:1], vcc
	s_cbranch_execz .LBB0_1304
	v_lshl_add_u64 v[74:75], v[68:69], 0, v[178:179]
	s_waitcnt lgkmcnt(0)
	v_cvt_pk_bf16_f32 v72, v72, v73
	global_store_dword v[74:75], v72, off
.LBB0_1304:
	s_or_b64 exec, exec, s[0:1]
	v_mul_f32_e32 v72, v59, v67
	s_waitcnt lgkmcnt(0)
	s_nop 1
	v_mov_b32_dpp v73, v72 quad_perm:[1,0,3,2] row_mask:0xf bank_mask:0xf
	s_and_saveexec_b64 s[0:1], vcc
	s_cbranch_execz .LBB0_1306
	v_lshl_add_u64 v[74:75], v[68:69], 0, v[178:179]
	s_waitcnt lgkmcnt(0)
	v_cvt_pk_bf16_f32 v72, v72, v73
	global_store_dword v[74:75], v72, off offset:64
; __device__ __forceinline__ unsigned cvt_pk_bf16(float lo, float hi) { unsigned r; asm volatile("v_cvt_pk_bf16_f32 %0, %1, %2" : "=v"(r) : "v"(lo), "v"(hi)); return r; }
; __device__ __forceinline__ float bf_lo(unsigned w) { return __uint_as_float(w << 16); }
; __device__ __forceinline__ float bf_hi(unsigned w) { return __uint_as_float(w & 0xffff0000u); }
; __device__ __forceinline__ int crow(int r, int hi) { return (r & 3) + 8 * (r >> 2) + 4 * hi; }
; template <int MODE> ...
;     ...
;     for (int r = 0; r < 16; ++r) { const int orow = qlo + crow(r, hi); const float rl = __builtin_amdgcn_rcpf(li_l[crow(r, hi)]);
; #pragma unroll
;         for (int d0 = 0; d0 < 4; ++d0) { float v = o[d0][r] * rl; float vn = __shfl_xor(v, 1);
;             if ((r32 & 1) == 0) { const int col = d0 * 32 + r32;
;                 if (MODE == 1) { const unsigned g = *(const unsigned*)(gate + (size_t)orow * 1024 + hoff + col); v *= bf_lo(g); vn *= bf_hi(g); }
;                 *(unsigned*)(Ob + (size_t)orow * DM + ocol0 + col) = cvt_pk_bf16(v, vn); } } }
.LBB0_1306:
	s_or_b64 exec, exec, s[0:1]
	v_mul_f32_e32 v72, v43, v67
	s_waitcnt lgkmcnt(0)
	s_nop 1
	v_mov_b32_dpp v73, v72 quad_perm:[1,0,3,2] row_mask:0xf bank_mask:0xf
	s_and_saveexec_b64 s[0:1], vcc
	s_cbranch_execz .LBB0_1308
	v_lshl_add_u64 v[74:75], v[68:69], 0, v[178:179]
	s_waitcnt lgkmcnt(0)
	v_cvt_pk_bf16_f32 v72, v72, v73
	global_store_dword v[74:75], v72, off offset:128
.LBB0_1308:
	s_or_b64 exec, exec, s[0:1]
	v_mul_f32_e32 v67, v27, v67
	s_nop 1
	v_mov_b32_dpp v72, v67 quad_perm:[1,0,3,2] row_mask:0xf bank_mask:0xf
	s_and_saveexec_b64 s[0:1], vcc
	s_cbranch_execz .LBB0_1310
	v_lshl_add_u64 v[68:69], v[68:69], 0, v[178:179]
	s_waitcnt lgkmcnt(0)
	v_cvt_pk_bf16_f32 v67, v67, v72
	global_store_dword v[68:69], v67, off offset:192
.LBB0_1310:
	s_or_b64 exec, exec, s[0:1]
	ds_read_b32 v67, v71 offset:72
	v_add_u32_e32 v68, 18, v66
	v_ashrrev_i32_e32 v69, 31, v68
	v_lshlrev_b64 v[68:69], 12, v[68:69]
	v_lshl_add_u64 v[68:69], s[22:23], 0, v[68:69]
	s_waitcnt lgkmcnt(0)
	v_rcp_f32_e32 v67, v67
	s_nop 0
	v_mul_f32_e32 v72, v12, v67
	s_nop 1
	v_mov_b32_dpp v73, v72 quad_perm:[1,0,3,2] row_mask:0xf bank_mask:0xf
	s_and_saveexec_b64 s[0:1], vcc
	s_cbranch_execz .LBB0_1312
	v_lshl_add_u64 v[74:75], v[68:69], 0, v[178:179]
	s_waitcnt lgkmcnt(0)
	v_cvt_pk_bf16_f32 v72, v72, v73
	global_store_dword v[74:75], v72, off
.LBB0_1312:
	s_or_b64 exec, exec, s[0:1]
	v_mul_f32_e32 v72, v60, v67
	s_waitcnt lgkmcnt(0)
	s_nop 1
	v_mov_b32_dpp v73, v72 quad_perm:[1,0,3,2] row_mask:0xf bank_mask:0xf
	s_and_saveexec_b64 s[0:1], vcc
	s_cbranch_execz .LBB0_1314
	v_lshl_add_u64 v[74:75], v[68:69], 0, v[178:179]
	s_waitcnt lgkmcnt(0)
	v_cvt_pk_bf16_f32 v72, v72, v73
	global_store_dword v[74:75], v72, off offset:64
.LBB0_1314:
	s_or_b64 exec, exec, s[0:1]
	v_mul_f32_e32 v72, v44, v67
	s_waitcnt lgkmcnt(0)
	s_nop 1
	v_mov_b32_dpp v73, v72 quad_perm:[1,0,3,2] row_mask:0xf bank_mask:0xf
	s_and_saveexec_b64 s[0:1], vcc
	s_cbranch_execz .LBB0_1316
	v_lshl_add_u64 v[74:75], v[68:69], 0, v[178:179]
	s_waitcnt lgkmcnt(0)
	v_cvt_pk_bf16_f32 v72, v72, v73
	global_store_dword v[74:75], v72, off offset:128
.LBB0_1316:
	s_or_b64 exec, exec, s[0:1]
	v_mul_f32_e32 v67, v28, v67
	s_nop 1
	v_mov_b32_dpp v72, v67 quad_perm:[1,0,3,2] row_mask:0xf bank_mask:0xf
	s_and_saveexec_b64 s[0:1], vcc
	s_cbranch_execz .LBB0_1318
	v_lshl_add_u64 v[68:69], v[68:69], 0, v[178:179]
	s_waitcnt lgkmcnt(0)
	v_cvt_pk_bf16_f32 v67, v67, v72
	global_store_dword v[68:69], v67, off offset:192
.LBB0_1318:
	s_or_b64 exec, exec, s[0:1]
	ds_read_b32 v67, v71 offset:76
	v_add_u32_e32 v68, 19, v66
	v_ashrrev_i32_e32 v69, 31, v68
	v_lshlrev_b64 v[68:69], 12, v[68:69]
	v_lshl_add_u64 v[68:69], s[22:23], 0, v[68:69]
	s_waitcnt lgkmcnt(0)
	v_rcp_f32_e32 v67, v67
	s_nop 0
	v_mul_f32_e32 v72, v13, v67
	s_nop 1
	v_mov_b32_dpp v73, v72 quad_perm:[1,0,3,2] row_mask:0xf bank_mask:0xf
	s_and_saveexec_b64 s[0:1], vcc
	s_cbranch_execz .LBB0_1320
	v_lshl_add_u64 v[74:75], v[68:69], 0, v[178:179]
	s_waitcnt lgkmcnt(0)
	v_cvt_pk_bf16_f32 v72, v72, v73
	global_store_dword v[74:75], v72, off
.LBB0_1320:
	s_or_b64 exec, exec, s[0:1]
	v_mul_f32_e32 v72, v61, v67
	s_waitcnt lgkmcnt(0)
	s_nop 1
	v_mov_b32_dpp v73, v72 quad_perm:[1,0,3,2] row_mask:0xf bank_mask:0xf
	s_and_saveexec_b64 s[0:1], vcc
	s_cbranch_execz .LBB0_1322
	v_lshl_add_u64 v[74:75], v[68:69], 0, v[178:179]
	s_waitcnt lgkmcnt(0)
	v_cvt_pk_bf16_f32 v72, v72, v73
	global_store_dword v[74:75], v72, off offset:64
.LBB0_1322:
	s_or_b64 exec, exec, s[0:1]
	v_mul_f32_e32 v72, v45, v67
	s_waitcnt lgkmcnt(0)
	s_nop 1
	v_mov_b32_dpp v73, v72 quad_perm:[1,0,3,2] row_mask:0xf bank_mask:0xf
	s_and_saveexec_b64 s[0:1], vcc
	s_cbranch_execz .LBB0_1324
	v_lshl_add_u64 v[74:75], v[68:69], 0, v[178:179]
	s_waitcnt lgkmcnt(0)
	v_cvt_pk_bf16_f32 v72, v72, v73
	global_store_dword v[74:75], v72, off offset:128
.LBB0_1324:
	s_or_b64 exec, exec, s[0:1]
	v_mul_f32_e32 v67, v29, v67
	s_nop 1
	v_mov_b32_dpp v72, v67 quad_perm:[1,0,3,2] row_mask:0xf bank_mask:0xf
	s_and_saveexec_b64 s[0:1], vcc
	s_cbranch_execz .LBB0_1326
	v_lshl_add_u64 v[68:69], v[68:69], 0, v[178:179]
	s_waitcnt lgkmcnt(0)
	v_cvt_pk_bf16_f32 v67, v67, v72
	global_store_dword v[68:69], v67, off offset:192
.LBB0_1326:
	s_or_b64 exec, exec, s[0:1]
	ds_read_b32 v67, v71 offset:96
	v_add_u32_e32 v68, 24, v66
	v_ashrrev_i32_e32 v69, 31, v68
	v_lshlrev_b64 v[68:69], 12, v[68:69]
	v_lshl_add_u64 v[68:69], s[22:23], 0, v[68:69]
	s_waitcnt lgkmcnt(0)
	v_rcp_f32_e32 v67, v67
	s_nop 0
	v_mul_f32_e32 v72, v14, v67
	s_nop 1
	v_mov_b32_dpp v73, v72 quad_perm:[1,0,3,2] row_mask:0xf bank_mask:0xf
	s_and_saveexec_b64 s[0:1], vcc
	s_cbranch_execz .LBB0_1328
	v_lshl_add_u64 v[74:75], v[68:69], 0, v[178:179]
	s_waitcnt lgkmcnt(0)
	v_cvt_pk_bf16_f32 v72, v72, v73
	global_store_dword v[74:75], v72, off
.LBB0_1328:
	s_or_b64 exec, exec, s[0:1]
	v_mul_f32_e32 v72, v62, v67
	s_waitcnt lgkmcnt(0)
	s_nop 1
	v_mov_b32_dpp v73, v72 quad_perm:[1,0,3,2] row_mask:0xf bank_mask:0xf
	s_and_saveexec_b64 s[0:1], vcc
	s_cbranch_execz .LBB0_1330
	v_lshl_add_u64 v[74:75], v[68:69], 0, v[178:179]
	s_waitcnt lgkmcnt(0)
	v_cvt_pk_bf16_f32 v72, v72, v73
	global_store_dword v[74:75], v72, off offset:64
.LBB0_1330:
	s_or_b64 exec, exec, s[0:1]
	v_mul_f32_e32 v72, v46, v67
	s_waitcnt lgkmcnt(0)
	s_nop 1
	v_mov_b32_dpp v73, v72 quad_perm:[1,0,3,2] row_mask:0xf bank_mask:0xf
	s_and_saveexec_b64 s[0:1], vcc
	s_cbranch_execz .LBB0_1332
	v_lshl_add_u64 v[74:75], v[68:69], 0, v[178:179]
	s_waitcnt lgkmcnt(0)
	v_cvt_pk_bf16_f32 v72, v72, v73
	global_store_dword v[74:75], v72, off offset:128
; __device__ __forceinline__ unsigned cvt_pk_bf16(float lo, float hi) { unsigned r; asm volatile("v_cvt_pk_bf16_f32 %0, %1, %2" : "=v"(r) : "v"(lo), "v"(hi)); return r; }
; __device__ __forceinline__ float bf_lo(unsigned w) { return __uint_as_float(w << 16); }
; __device__ __forceinline__ float bf_hi(unsigned w) { return __uint_as_float(w & 0xffff0000u); }
; __device__ __forceinline__ int crow(int r, int hi) { return (r & 3) + 8 * (r >> 2) + 4 * hi; }
; template <int MODE> ...
;     ...
;     for (int r = 0; r < 16; ++r) { const int orow = qlo + crow(r, hi); const float rl = __builtin_amdgcn_rcpf(li_l[crow(r, hi)]);
; #pragma unroll
;         for (int d0 = 0; d0 < 4; ++d0) { float v = o[d0][r] * rl; float vn = __shfl_xor(v, 1);
;             if ((r32 & 1) == 0) { const int col = d0 * 32 + r32;
;                 if (MODE == 1) { const unsigned g = *(const unsigned*)(gate + (size_t)orow * 1024 + hoff + col); v *= bf_lo(g); vn *= bf_hi(g); }
;                 *(unsigned*)(Ob + (size_t)orow * DM + ocol0 + col) = cvt_pk_bf16(v, vn); } } }
.LBB0_1332:
	s_or_b64 exec, exec, s[0:1]
	v_mul_f32_e32 v67, v30, v67
	s_nop 1
	v_mov_b32_dpp v72, v67 quad_perm:[1,0,3,2] row_mask:0xf bank_mask:0xf
	s_and_saveexec_b64 s[0:1], vcc
	s_cbranch_execz .LBB0_1334
	v_lshl_add_u64 v[68:69], v[68:69], 0, v[178:179]
	s_waitcnt lgkmcnt(0)
	v_cvt_pk_bf16_f32 v67, v67, v72
	global_store_dword v[68:69], v67, off offset:192
.LBB0_1334:
	s_or_b64 exec, exec, s[0:1]
	ds_read_b32 v67, v71 offset:100
	v_add_u32_e32 v68, 25, v66
	v_ashrrev_i32_e32 v69, 31, v68
	v_lshlrev_b64 v[68:69], 12, v[68:69]
	v_lshl_add_u64 v[68:69], s[22:23], 0, v[68:69]
	s_waitcnt lgkmcnt(0)
	v_rcp_f32_e32 v67, v67
	s_nop 0
	v_mul_f32_e32 v72, v15, v67
	s_nop 1
	v_mov_b32_dpp v73, v72 quad_perm:[1,0,3,2] row_mask:0xf bank_mask:0xf
	s_and_saveexec_b64 s[0:1], vcc
	s_cbranch_execz .LBB0_1336
	v_lshl_add_u64 v[74:75], v[68:69], 0, v[178:179]
	s_waitcnt lgkmcnt(0)
	v_cvt_pk_bf16_f32 v72, v72, v73
	global_store_dword v[74:75], v72, off
.LBB0_1336:
	s_or_b64 exec, exec, s[0:1]
	v_mul_f32_e32 v72, v63, v67
	s_waitcnt lgkmcnt(0)
	s_nop 1
	v_mov_b32_dpp v73, v72 quad_perm:[1,0,3,2] row_mask:0xf bank_mask:0xf
	s_and_saveexec_b64 s[0:1], vcc
	s_cbranch_execz .LBB0_1338
	v_lshl_add_u64 v[74:75], v[68:69], 0, v[178:179]
	s_waitcnt lgkmcnt(0)
	v_cvt_pk_bf16_f32 v72, v72, v73
	global_store_dword v[74:75], v72, off offset:64
.LBB0_1338:
	s_or_b64 exec, exec, s[0:1]
	v_mul_f32_e32 v72, v47, v67
	s_waitcnt lgkmcnt(0)
	s_nop 1
	v_mov_b32_dpp v73, v72 quad_perm:[1,0,3,2] row_mask:0xf bank_mask:0xf
	s_and_saveexec_b64 s[0:1], vcc
	s_cbranch_execz .LBB0_1340
	v_lshl_add_u64 v[74:75], v[68:69], 0, v[178:179]
	s_waitcnt lgkmcnt(0)
	v_cvt_pk_bf16_f32 v72, v72, v73
	global_store_dword v[74:75], v72, off offset:128
.LBB0_1340:
	s_or_b64 exec, exec, s[0:1]
	v_mul_f32_e32 v67, v31, v67
	s_nop 1
	v_mov_b32_dpp v72, v67 quad_perm:[1,0,3,2] row_mask:0xf bank_mask:0xf
	s_and_saveexec_b64 s[0:1], vcc
	s_cbranch_execz .LBB0_1342
	v_lshl_add_u64 v[68:69], v[68:69], 0, v[178:179]
	s_waitcnt lgkmcnt(0)
	v_cvt_pk_bf16_f32 v67, v67, v72
	global_store_dword v[68:69], v67, off offset:192
.LBB0_1342:
	s_or_b64 exec, exec, s[0:1]
	ds_read_b32 v67, v71 offset:104
	v_add_u32_e32 v68, 26, v66
	v_ashrrev_i32_e32 v69, 31, v68
	v_lshlrev_b64 v[68:69], 12, v[68:69]
	v_lshl_add_u64 v[68:69], s[22:23], 0, v[68:69]
	s_waitcnt lgkmcnt(0)
	v_rcp_f32_e32 v67, v67
	s_nop 0
	v_mul_f32_e32 v72, v16, v67
	s_nop 1
	v_mov_b32_dpp v73, v72 quad_perm:[1,0,3,2] row_mask:0xf bank_mask:0xf
	s_and_saveexec_b64 s[0:1], vcc
	s_cbranch_execz .LBB0_1344
	v_lshl_add_u64 v[74:75], v[68:69], 0, v[178:179]
	s_waitcnt lgkmcnt(0)
	v_cvt_pk_bf16_f32 v72, v72, v73
	global_store_dword v[74:75], v72, off
.LBB0_1344:
	s_or_b64 exec, exec, s[0:1]
	v_mul_f32_e32 v72, v64, v67
	s_waitcnt lgkmcnt(0)
	s_nop 1
	v_mov_b32_dpp v73, v72 quad_perm:[1,0,3,2] row_mask:0xf bank_mask:0xf
	s_and_saveexec_b64 s[0:1], vcc
	s_cbranch_execz .LBB0_1346
	v_lshl_add_u64 v[74:75], v[68:69], 0, v[178:179]
	s_waitcnt lgkmcnt(0)
	v_cvt_pk_bf16_f32 v72, v72, v73
	global_store_dword v[74:75], v72, off offset:64
.LBB0_1346:
	s_or_b64 exec, exec, s[0:1]
	v_mul_f32_e32 v72, v48, v67
	s_waitcnt lgkmcnt(0)
	s_nop 1
	v_mov_b32_dpp v73, v72 quad_perm:[1,0,3,2] row_mask:0xf bank_mask:0xf
	s_and_saveexec_b64 s[0:1], vcc
	s_cbranch_execz .LBB0_1348
	v_lshl_add_u64 v[74:75], v[68:69], 0, v[178:179]
	s_waitcnt lgkmcnt(0)
	v_cvt_pk_bf16_f32 v72, v72, v73
	global_store_dword v[74:75], v72, off offset:128
.LBB0_1348:
	s_or_b64 exec, exec, s[0:1]
	v_mul_f32_e32 v67, v32, v67
	s_nop 1
	v_mov_b32_dpp v72, v67 quad_perm:[1,0,3,2] row_mask:0xf bank_mask:0xf
	s_and_saveexec_b64 s[0:1], vcc
	s_cbranch_execz .LBB0_1350
	v_lshl_add_u64 v[68:69], v[68:69], 0, v[178:179]
	s_waitcnt lgkmcnt(0)
	v_cvt_pk_bf16_f32 v67, v67, v72
	global_store_dword v[68:69], v67, off offset:192
.LBB0_1350:
	s_or_b64 exec, exec, s[0:1]
	ds_read_b32 v67, v71 offset:108
	v_add_u32_e32 v66, 27, v66
	s_waitcnt lgkmcnt(0)
	v_rcp_f32_e32 v68, v67
	v_ashrrev_i32_e32 v67, 31, v66
	v_lshlrev_b64 v[66:67], 12, v[66:67]
	v_lshl_add_u64 v[66:67], s[22:23], 0, v[66:67]
	v_mul_f32_e32 v69, v17, v68
	s_nop 1
	v_mov_b32_dpp v71, v69 quad_perm:[1,0,3,2] row_mask:0xf bank_mask:0xf
	s_and_saveexec_b64 s[0:1], vcc
	s_cbranch_execz .LBB0_1352
	v_lshl_add_u64 v[72:73], v[66:67], 0, v[178:179]
	s_waitcnt lgkmcnt(0)
	v_cvt_pk_bf16_f32 v69, v69, v71
	global_store_dword v[72:73], v69, off
.LBB0_1352:
	s_or_b64 exec, exec, s[0:1]
	v_mul_f32_e32 v69, v65, v68
	s_waitcnt lgkmcnt(0)
	s_nop 1
	v_mov_b32_dpp v71, v69 quad_perm:[1,0,3,2] row_mask:0xf bank_mask:0xf
	s_and_saveexec_b64 s[0:1], vcc
	s_cbranch_execz .LBB0_1354
	v_lshl_add_u64 v[72:73], v[66:67], 0, v[178:179]
	s_waitcnt lgkmcnt(0)
	v_cvt_pk_bf16_f32 v69, v69, v71
	global_store_dword v[72:73], v69, off offset:64
.LBB0_1354:
	s_or_b64 exec, exec, s[0:1]
	v_mul_f32_e32 v69, v49, v68
	s_waitcnt lgkmcnt(0)
	s_nop 1
	v_mov_b32_dpp v71, v69 quad_perm:[1,0,3,2] row_mask:0xf bank_mask:0xf
	s_and_saveexec_b64 s[0:1], vcc
	s_cbranch_execz .LBB0_1356
	v_lshl_add_u64 v[72:73], v[66:67], 0, v[178:179]
	s_waitcnt lgkmcnt(0)
	v_cvt_pk_bf16_f32 v69, v69, v71
	global_store_dword v[72:73], v69, off offset:128
.LBB0_1356:
	s_or_b64 exec, exec, s[0:1]
	v_mul_f32_e32 v68, v33, v68
	s_nop 1
	v_mov_b32_dpp v69, v68 quad_perm:[1,0,3,2] row_mask:0xf bank_mask:0xf
	s_and_saveexec_b64 s[0:1], vcc
	s_xor_b64 s[0:1], exec, s[0:1]
	s_cbranch_execz .LBB0_1358
	v_lshl_add_u64 v[66:67], v[66:67], 0, v[178:179]
	s_waitcnt lgkmcnt(0)
	v_cvt_pk_bf16_f32 v68, v68, v69
	global_store_dword v[66:67], v68, off offset:192

; __device__ __forceinline__ unsigned cvt_pk_bf16(float lo, float hi) { unsigned r; asm volatile("v_cvt_pk_bf16_f32 %0, %1, %2" : "=v"(r) : "v"(lo), "v"(hi)); return r; }
; __device__ __forceinline__ float bf_lo(unsigned w) { return __uint_as_float(w << 16); }
; __device__ __forceinline__ float bf_hi(unsigned w) { return __uint_as_float(w & 0xffff0000u); }
; __device__ __forceinline__ int crow(int r, int hi) { return (r & 3) + 8 * (r >> 2) + 4 * hi; }
; template <int MODE> ...
;     ...
;     if (hi == 0) li_l[r32] = l_reg; asm volatile("s_waitcnt lgkmcnt(0)" ::: "memory");
; #pragma unroll
;     for (int r = 0; r < 16; ++r) { const int orow = qlo + crow(r, hi); const float rl = __builtin_amdgcn_rcpf(li_l[crow(r, hi)]);
; #pragma unroll
;         for (int d0 = 0; d0 < 4; ++d0) { float v = o[d0][r] * rl; float vn = __shfl_xor(v, 1);
;             if ((r32 & 1) == 0) { const int col = d0 * 32 + r32;
;                 if (MODE == 1) { const unsigned g = *(const unsigned*)(gate + (size_t)orow * 1024 + hoff + col); v *= bf_lo(g); vn *= bf_hi(g); }
;                 *(unsigned*)(Ob + (size_t)orow * DM + ocol0 + col) = cvt_pk_bf16(v, vn); } } }
.LBB0_1410:
	s_and_saveexec_b64 s[0:1], s[4:5]
	v_readlane_b32 s10, v240, 8
	ds_write_b32 v163, v178
	s_or_b64 exec, exec, s[0:1]
	s_waitcnt lgkmcnt(0)
	ds_read_b32 v5, v160
	v_and_b32_e32 v4, 64, v1
	v_xor_b32_e32 v2, 1, v1
	v_add_u32_e32 v4, 64, v4
	v_cmp_lt_i32_e32 vcc, v2, v4
	s_waitcnt lgkmcnt(0)
	v_rcp_f32_e32 v11, v5
	v_add_u32_e32 v4, s10, v162
	v_cndmask_b32_e32 v2, v1, v2, vcc
	v_lshlrev_b32_e32 v10, 2, v2
	v_mul_f32_e32 v12, v66, v11
	s_nop 1
	v_mov_b32_dpp v13, v12 quad_perm:[1,0,3,2] row_mask:0xf bank_mask:0xf
	v_ashrrev_i32_e32 v5, 31, v4
	v_readlane_b32 s6, v240, 14
	v_lshlrev_b64 v[6:7], 11, v[4:5]
	v_readlane_b32 s7, v240, 15
	v_readlane_b32 s8, v240, 16
	v_readlane_b32 s9, v240, 17
	v_lshl_add_u64 v[8:9], s[6:7], 0, v[6:7]
	v_lshlrev_b64 v[6:7], 12, v[4:5]
	v_lshl_add_u64 v[6:7], s[8:9], 0, v[6:7]
	v_lshlrev_b32_e32 v2, 1, v161
	s_and_saveexec_b64 s[0:1], s[2:3]
	s_cbranch_execz .LBB0_1414
	v_lshl_add_u64 v[14:15], v[8:9], 0, v[2:3]
	global_load_dword v5, v[14:15], off
	s_waitcnt vmcnt(0)
	v_lshlrev_b32_e32 v14, 16, v5
	v_and_b32_e32 v5, 0xffff0000, v5
	v_mul_f32_e32 v12, v12, v14
	s_waitcnt lgkmcnt(0)
	v_mul_f32_e32 v5, v13, v5
	v_cvt_pk_bf16_f32 v5, v12, v5
	v_lshl_add_u64 v[12:13], v[6:7], 0, v[2:3]
	global_store_dword v[12:13], v5, off
.LBB0_1414:
	s_or_b64 exec, exec, s[0:1]
	v_mul_f32_e32 v5, v50, v11
	s_nop 1
	v_mov_b32_dpp v12, v5 quad_perm:[1,0,3,2] row_mask:0xf bank_mask:0xf
	s_and_saveexec_b64 s[0:1], s[2:3]
	s_cbranch_execz .LBB0_1416
	v_lshl_add_u64 v[14:15], v[8:9], 0, v[2:3]
	s_waitcnt lgkmcnt(0)
	global_load_dword v13, v[14:15], off offset:64
	s_waitcnt vmcnt(0)
	v_lshlrev_b32_e32 v14, 16, v13
	v_and_b32_e32 v13, 0xffff0000, v13
	v_mul_f32_e32 v5, v5, v14
	s_waitcnt lgkmcnt(0)
	v_mul_f32_e32 v12, v12, v13
	v_cvt_pk_bf16_f32 v5, v5, v12
	v_lshl_add_u64 v[12:13], v[6:7], 0, v[2:3]
	global_store_dword v[12:13], v5, off offset:64
.LBB0_1416:
	s_or_b64 exec, exec, s[0:1]
	v_mul_f32_e32 v5, v34, v11
	s_waitcnt lgkmcnt(0)
	s_nop 1
	v_mov_b32_dpp v12, v5 quad_perm:[1,0,3,2] row_mask:0xf bank_mask:0xf
	s_and_saveexec_b64 s[0:1], s[2:3]
	s_cbranch_execz .LBB0_1418
	v_lshl_add_u64 v[14:15], v[8:9], 0, v[2:3]
	global_load_dword v13, v[14:15], off offset:128
	s_waitcnt vmcnt(0)
	v_lshlrev_b32_e32 v14, 16, v13
	v_and_b32_e32 v13, 0xffff0000, v13
	v_mul_f32_e32 v5, v5, v14
	s_waitcnt lgkmcnt(0)
	v_mul_f32_e32 v12, v12, v13
	v_cvt_pk_bf16_f32 v5, v5, v12
	v_lshl_add_u64 v[12:13], v[6:7], 0, v[2:3]
	global_store_dword v[12:13], v5, off offset:128
.LBB0_1418:
	s_or_b64 exec, exec, s[0:1]
	v_mul_f32_e32 v5, v18, v11
	s_nop 1
	v_mov_b32_dpp v11, v5 quad_perm:[1,0,3,2] row_mask:0xf bank_mask:0xf
	s_and_saveexec_b64 s[0:1], s[2:3]
	s_cbranch_execz .LBB0_1420
	v_lshl_add_u64 v[8:9], v[8:9], 0, v[2:3]
	global_load_dword v8, v[8:9], off offset:192
	v_lshl_add_u64 v[6:7], v[6:7], 0, v[2:3]
	s_waitcnt vmcnt(0)
	v_lshlrev_b32_e32 v9, 16, v8
	v_and_b32_e32 v8, 0xffff0000, v8
	v_mul_f32_e32 v5, v5, v9
	s_waitcnt lgkmcnt(0)
	v_mul_f32_e32 v8, v11, v8
	v_cvt_pk_bf16_f32 v5, v5, v8
	global_store_dword v[6:7], v5, off offset:192
.LBB0_1420:
	s_or_b64 exec, exec, s[0:1]
	ds_read_b32 v5, v160 offset:4
	v_add3_u32 v6, s10, v162, 1
	v_ashrrev_i32_e32 v7, 31, v6
	v_lshlrev_b64 v[8:9], 11, v[6:7]
	v_lshlrev_b64 v[6:7], 12, v[6:7]
	s_waitcnt lgkmcnt(0)
	v_rcp_f32_e32 v5, v5
	v_lshl_add_u64 v[8:9], s[6:7], 0, v[8:9]
	v_lshl_add_u64 v[6:7], s[8:9], 0, v[6:7]
	v_lshl_add_u64 v[242:243], v[8:9], 0, v[2:3]
	global_load_dword v244, v[242:243], off
	global_load_dword v245, v[242:243], off offset:64
	global_load_dword v246, v[242:243], off offset:128
	global_load_dword v247, v[242:243], off offset:192
	v_mul_f32_e32 v11, v67, v5
	s_nop 1
	v_mov_b32_dpp v12, v11 quad_perm:[1,0,3,2] row_mask:0xf bank_mask:0xf
	s_and_saveexec_b64 s[0:1], s[2:3]
	s_cbranch_execz .LBB0_1422
	v_lshl_add_u64 v[14:15], v[8:9], 0, v[2:3]
	s_waitcnt vmcnt(0)
	v_mov_b32_e32 v13, v244
	v_lshlrev_b32_e32 v14, 16, v13
	v_and_b32_e32 v13, 0xffff0000, v13
	v_mul_f32_e32 v11, v11, v14
	s_waitcnt lgkmcnt(0)
	v_mul_f32_e32 v12, v12, v13
	v_cvt_pk_bf16_f32 v11, v11, v12
	v_lshl_add_u64 v[12:13], v[6:7], 0, v[2:3]
	global_store_dword v[12:13], v11, off
.LBB0_1422:
	s_or_b64 exec, exec, s[0:1]
	v_mul_f32_e32 v11, v51, v5
	s_waitcnt lgkmcnt(0)
	s_nop 1
	v_mov_b32_dpp v12, v11 quad_perm:[1,0,3,2] row_mask:0xf bank_mask:0xf
	s_and_saveexec_b64 s[0:1], s[2:3]
	s_cbranch_execz .LBB0_1424
	v_lshl_add_u64 v[14:15], v[8:9], 0, v[2:3]
	v_mov_b32_e32 v13, v245
	v_lshlrev_b32_e32 v14, 16, v13
	v_and_b32_e32 v13, 0xffff0000, v13
	v_mul_f32_e32 v11, v11, v14
	s_waitcnt lgkmcnt(0)
	v_mul_f32_e32 v12, v12, v13
	v_cvt_pk_bf16_f32 v11, v11, v12
	v_lshl_add_u64 v[12:13], v[6:7], 0, v[2:3]
	global_store_dword v[12:13], v11, off offset:64
.LBB0_1424:
	s_or_b64 exec, exec, s[0:1]
	v_mul_f32_e32 v11, v35, v5
	s_waitcnt lgkmcnt(0)
	s_nop 1
	v_mov_b32_dpp v12, v11 quad_perm:[1,0,3,2] row_mask:0xf bank_mask:0xf
	s_and_saveexec_b64 s[0:1], s[2:3]
	s_cbranch_execz .LBB0_1426
	v_lshl_add_u64 v[14:15], v[8:9], 0, v[2:3]
	v_mov_b32_e32 v13, v246
	v_lshlrev_b32_e32 v14, 16, v13
	v_and_b32_e32 v13, 0xffff0000, v13
	v_mul_f32_e32 v11, v11, v14
	s_waitcnt lgkmcnt(0)
	v_mul_f32_e32 v12, v12, v13
	v_cvt_pk_bf16_f32 v11, v11, v12
	v_lshl_add_u64 v[12:13], v[6:7], 0, v[2:3]
	global_store_dword v[12:13], v11, off offset:128
.LBB0_1426:
	s_or_b64 exec, exec, s[0:1]
	v_mul_f32_e32 v5, v19, v5
	s_nop 1
	v_mov_b32_dpp v11, v5 quad_perm:[1,0,3,2] row_mask:0xf bank_mask:0xf
	s_and_saveexec_b64 s[0:1], s[2:3]
	s_cbranch_execz .LBB0_1428
	v_lshl_add_u64 v[8:9], v[8:9], 0, v[2:3]
	v_lshl_add_u64 v[6:7], v[6:7], 0, v[2:3]
	v_mov_b32_e32 v8, v247
	v_lshlrev_b32_e32 v9, 16, v8
	v_and_b32_e32 v8, 0xffff0000, v8
	v_mul_f32_e32 v5, v5, v9
	s_waitcnt lgkmcnt(0)
	v_mul_f32_e32 v8, v11, v8
	v_cvt_pk_bf16_f32 v5, v5, v8
	global_store_dword v[6:7], v5, off offset:192
; __device__ __forceinline__ unsigned cvt_pk_bf16(float lo, float hi) { unsigned r; asm volatile("v_cvt_pk_bf16_f32 %0, %1, %2" : "=v"(r) : "v"(lo), "v"(hi)); return r; }
; __device__ __forceinline__ float bf_lo(unsigned w) { return __uint_as_float(w << 16); }
; __device__ __forceinline__ float bf_hi(unsigned w) { return __uint_as_float(w & 0xffff0000u); }
; __device__ __forceinline__ int crow(int r, int hi) { return (r & 3) + 8 * (r >> 2) + 4 * hi; }
; template <int MODE> ...
;     ...
;     for (int r = 0; r < 16; ++r) { const int orow = qlo + crow(r, hi); const float rl = __builtin_amdgcn_rcpf(li_l[crow(r, hi)]);
; #pragma unroll
;         for (int d0 = 0; d0 < 4; ++d0) { float v = o[d0][r] * rl; float vn = __shfl_xor(v, 1);
;             if ((r32 & 1) == 0) { const int col = d0 * 32 + r32;
;                 if (MODE == 1) { const unsigned g = *(const unsigned*)(gate + (size_t)orow * 1024 + hoff + col); v *= bf_lo(g); vn *= bf_hi(g); }
;                 *(unsigned*)(Ob + (size_t)orow * DM + ocol0 + col) = cvt_pk_bf16(v, vn); } } }
.LBB0_1428:
	s_or_b64 exec, exec, s[0:1]
	ds_read_b32 v5, v160 offset:8
	v_add3_u32 v6, s10, v162, 2
	v_ashrrev_i32_e32 v7, 31, v6
	v_lshlrev_b64 v[8:9], 11, v[6:7]
	v_lshlrev_b64 v[6:7], 12, v[6:7]
	s_waitcnt lgkmcnt(0)
	v_rcp_f32_e32 v5, v5
	v_lshl_add_u64 v[8:9], s[6:7], 0, v[8:9]
	v_lshl_add_u64 v[6:7], s[8:9], 0, v[6:7]
	v_lshl_add_u64 v[242:243], v[8:9], 0, v[2:3]
	global_load_dword v244, v[242:243], off
	global_load_dword v245, v[242:243], off offset:64
	global_load_dword v246, v[242:243], off offset:128
	global_load_dword v247, v[242:243], off offset:192
	v_mul_f32_e32 v11, v68, v5
	s_nop 1
	v_mov_b32_dpp v12, v11 quad_perm:[1,0,3,2] row_mask:0xf bank_mask:0xf
	s_and_saveexec_b64 s[0:1], s[2:3]
	s_cbranch_execz .LBB0_1430
	v_lshl_add_u64 v[14:15], v[8:9], 0, v[2:3]
	s_waitcnt vmcnt(0)
	v_mov_b32_e32 v13, v244
	v_lshlrev_b32_e32 v14, 16, v13
	v_and_b32_e32 v13, 0xffff0000, v13
	v_mul_f32_e32 v11, v11, v14
	s_waitcnt lgkmcnt(0)
	v_mul_f32_e32 v12, v12, v13
	v_cvt_pk_bf16_f32 v11, v11, v12
	v_lshl_add_u64 v[12:13], v[6:7], 0, v[2:3]
	global_store_dword v[12:13], v11, off
.LBB0_1430:
	s_or_b64 exec, exec, s[0:1]
	v_mul_f32_e32 v11, v52, v5
	s_waitcnt lgkmcnt(0)
	s_nop 1
	v_mov_b32_dpp v12, v11 quad_perm:[1,0,3,2] row_mask:0xf bank_mask:0xf
	s_and_saveexec_b64 s[0:1], s[2:3]
	s_cbranch_execz .LBB0_1432
	v_lshl_add_u64 v[14:15], v[8:9], 0, v[2:3]
	v_mov_b32_e32 v13, v245
	v_lshlrev_b32_e32 v14, 16, v13
	v_and_b32_e32 v13, 0xffff0000, v13
	v_mul_f32_e32 v11, v11, v14
	s_waitcnt lgkmcnt(0)
	v_mul_f32_e32 v12, v12, v13
	v_cvt_pk_bf16_f32 v11, v11, v12
	v_lshl_add_u64 v[12:13], v[6:7], 0, v[2:3]
	global_store_dword v[12:13], v11, off offset:64
.LBB0_1432:
	s_or_b64 exec, exec, s[0:1]
	v_mul_f32_e32 v11, v36, v5
	s_waitcnt lgkmcnt(0)
	s_nop 1
	v_mov_b32_dpp v12, v11 quad_perm:[1,0,3,2] row_mask:0xf bank_mask:0xf
	s_and_saveexec_b64 s[0:1], s[2:3]
	s_cbranch_execz .LBB0_1434
	v_lshl_add_u64 v[14:15], v[8:9], 0, v[2:3]
	v_mov_b32_e32 v13, v246
	v_lshlrev_b32_e32 v14, 16, v13
	v_and_b32_e32 v13, 0xffff0000, v13
	v_mul_f32_e32 v11, v11, v14
	s_waitcnt lgkmcnt(0)
	v_mul_f32_e32 v12, v12, v13
	v_cvt_pk_bf16_f32 v11, v11, v12
	v_lshl_add_u64 v[12:13], v[6:7], 0, v[2:3]
	global_store_dword v[12:13], v11, off offset:128
.LBB0_1434:
	s_or_b64 exec, exec, s[0:1]
	v_mul_f32_e32 v5, v20, v5
	s_nop 1
	v_mov_b32_dpp v11, v5 quad_perm:[1,0,3,2] row_mask:0xf bank_mask:0xf
	s_and_saveexec_b64 s[0:1], s[2:3]
	s_cbranch_execz .LBB0_1436
	v_lshl_add_u64 v[8:9], v[8:9], 0, v[2:3]
	v_lshl_add_u64 v[6:7], v[6:7], 0, v[2:3]
	v_mov_b32_e32 v8, v247
	v_lshlrev_b32_e32 v9, 16, v8
	v_and_b32_e32 v8, 0xffff0000, v8
	v_mul_f32_e32 v5, v5, v9
	s_waitcnt lgkmcnt(0)
	v_mul_f32_e32 v8, v11, v8
	v_cvt_pk_bf16_f32 v5, v5, v8
	global_store_dword v[6:7], v5, off offset:192
.LBB0_1436:
	s_or_b64 exec, exec, s[0:1]
	ds_read_b32 v5, v160 offset:12
	v_add3_u32 v6, s10, v162, 3
	v_ashrrev_i32_e32 v7, 31, v6
	v_lshlrev_b64 v[8:9], 11, v[6:7]
	v_lshlrev_b64 v[6:7], 12, v[6:7]
	s_waitcnt lgkmcnt(0)
	v_rcp_f32_e32 v5, v5
	v_lshl_add_u64 v[8:9], s[6:7], 0, v[8:9]
	v_lshl_add_u64 v[6:7], s[8:9], 0, v[6:7]
	v_lshl_add_u64 v[242:243], v[8:9], 0, v[2:3]
	global_load_dword v244, v[242:243], off
	global_load_dword v245, v[242:243], off offset:64
	global_load_dword v246, v[242:243], off offset:128
	global_load_dword v247, v[242:243], off offset:192
	v_mul_f32_e32 v11, v69, v5
	s_nop 1
	v_mov_b32_dpp v12, v11 quad_perm:[1,0,3,2] row_mask:0xf bank_mask:0xf
	s_and_saveexec_b64 s[0:1], s[2:3]
	s_cbranch_execz .LBB0_1438
	v_lshl_add_u64 v[14:15], v[8:9], 0, v[2:3]
	s_waitcnt vmcnt(0)
	v_mov_b32_e32 v13, v244
	v_lshlrev_b32_e32 v14, 16, v13
	v_and_b32_e32 v13, 0xffff0000, v13
	v_mul_f32_e32 v11, v11, v14
	s_waitcnt lgkmcnt(0)
	v_mul_f32_e32 v12, v12, v13
	v_cvt_pk_bf16_f32 v11, v11, v12
	v_lshl_add_u64 v[12:13], v[6:7], 0, v[2:3]
	global_store_dword v[12:13], v11, off
.LBB0_1438:
	s_or_b64 exec, exec, s[0:1]
	v_mul_f32_e32 v11, v53, v5
	s_waitcnt lgkmcnt(0)
	s_nop 1
	v_mov_b32_dpp v12, v11 quad_perm:[1,0,3,2] row_mask:0xf bank_mask:0xf
	s_and_saveexec_b64 s[0:1], s[2:3]
	s_cbranch_execz .LBB0_1440
	v_lshl_add_u64 v[14:15], v[8:9], 0, v[2:3]
	v_mov_b32_e32 v13, v245
	v_lshlrev_b32_e32 v14, 16, v13
	v_and_b32_e32 v13, 0xffff0000, v13
	v_mul_f32_e32 v11, v11, v14
	s_waitcnt lgkmcnt(0)
	v_mul_f32_e32 v12, v12, v13
	v_cvt_pk_bf16_f32 v11, v11, v12
	v_lshl_add_u64 v[12:13], v[6:7], 0, v[2:3]
	global_store_dword v[12:13], v11, off offset:64
.LBB0_1440:
	s_or_b64 exec, exec, s[0:1]
	v_mul_f32_e32 v11, v37, v5
	s_waitcnt lgkmcnt(0)
	s_nop 1
	v_mov_b32_dpp v12, v11 quad_perm:[1,0,3,2] row_mask:0xf bank_mask:0xf
	s_and_saveexec_b64 s[0:1], s[2:3]
	s_cbranch_execz .LBB0_1442
	v_lshl_add_u64 v[14:15], v[8:9], 0, v[2:3]
	v_mov_b32_e32 v13, v246
	v_lshlrev_b32_e32 v14, 16, v13
	v_and_b32_e32 v13, 0xffff0000, v13
	v_mul_f32_e32 v11, v11, v14
	s_waitcnt lgkmcnt(0)
	v_mul_f32_e32 v12, v12, v13
	v_cvt_pk_bf16_f32 v11, v11, v12
	v_lshl_add_u64 v[12:13], v[6:7], 0, v[2:3]
	global_store_dword v[12:13], v11, off offset:128
.LBB0_1442:
	s_or_b64 exec, exec, s[0:1]
	v_mul_f32_e32 v5, v21, v5
	s_nop 1
	v_mov_b32_dpp v11, v5 quad_perm:[1,0,3,2] row_mask:0xf bank_mask:0xf
	s_and_saveexec_b64 s[0:1], s[2:3]
	s_cbranch_execz .LBB0_1444
	v_lshl_add_u64 v[8:9], v[8:9], 0, v[2:3]
	v_lshl_add_u64 v[6:7], v[6:7], 0, v[2:3]
	v_mov_b32_e32 v8, v247
	v_lshlrev_b32_e32 v9, 16, v8
	v_and_b32_e32 v8, 0xffff0000, v8
	v_mul_f32_e32 v5, v5, v9
	s_waitcnt lgkmcnt(0)
	v_mul_f32_e32 v8, v11, v8
	v_cvt_pk_bf16_f32 v5, v5, v8
	global_store_dword v[6:7], v5, off offset:192
; __device__ __forceinline__ unsigned cvt_pk_bf16(float lo, float hi) { unsigned r; asm volatile("v_cvt_pk_bf16_f32 %0, %1, %2" : "=v"(r) : "v"(lo), "v"(hi)); return r; }
; __device__ __forceinline__ float bf_lo(unsigned w) { return __uint_as_float(w << 16); }
; __device__ __forceinline__ float bf_hi(unsigned w) { return __uint_as_float(w & 0xffff0000u); }
; __device__ __forceinline__ int crow(int r, int hi) { return (r & 3) + 8 * (r >> 2) + 4 * hi; }
; template <int MODE> ...
;     ...
;     for (int r = 0; r < 16; ++r) { const int orow = qlo + crow(r, hi); const float rl = __builtin_amdgcn_rcpf(li_l[crow(r, hi)]);
; #pragma unroll
;         for (int d0 = 0; d0 < 4; ++d0) { float v = o[d0][r] * rl; float vn = __shfl_xor(v, 1);
;             if ((r32 & 1) == 0) { const int col = d0 * 32 + r32;
;                 if (MODE == 1) { const unsigned g = *(const unsigned*)(gate + (size_t)orow * 1024 + hoff + col); v *= bf_lo(g); vn *= bf_hi(g); }
;                 *(unsigned*)(Ob + (size_t)orow * DM + ocol0 + col) = cvt_pk_bf16(v, vn); } } }
.LBB0_1444:
	s_or_b64 exec, exec, s[0:1]
	ds_read_b32 v5, v160 offset:32
	v_add_u32_e32 v6, 8, v4
	v_ashrrev_i32_e32 v7, 31, v6
	v_lshlrev_b64 v[8:9], 11, v[6:7]
	v_lshlrev_b64 v[6:7], 12, v[6:7]
	s_waitcnt lgkmcnt(0)
	v_rcp_f32_e32 v5, v5
	v_lshl_add_u64 v[8:9], s[6:7], 0, v[8:9]
	v_lshl_add_u64 v[6:7], s[8:9], 0, v[6:7]
	v_lshl_add_u64 v[242:243], v[8:9], 0, v[2:3]
	global_load_dword v244, v[242:243], off
	global_load_dword v245, v[242:243], off offset:64
	global_load_dword v246, v[242:243], off offset:128
	global_load_dword v247, v[242:243], off offset:192
	v_mul_f32_e32 v11, v70, v5
	s_nop 1
	v_mov_b32_dpp v12, v11 quad_perm:[1,0,3,2] row_mask:0xf bank_mask:0xf
	s_and_saveexec_b64 s[0:1], s[2:3]
	s_cbranch_execz .LBB0_1446
	v_lshl_add_u64 v[14:15], v[8:9], 0, v[2:3]
	s_waitcnt vmcnt(0)
	v_mov_b32_e32 v13, v244
	v_lshlrev_b32_e32 v14, 16, v13
	v_and_b32_e32 v13, 0xffff0000, v13
	v_mul_f32_e32 v11, v11, v14
	s_waitcnt lgkmcnt(0)
	v_mul_f32_e32 v12, v12, v13
	v_cvt_pk_bf16_f32 v11, v11, v12
	v_lshl_add_u64 v[12:13], v[6:7], 0, v[2:3]
	global_store_dword v[12:13], v11, off
.LBB0_1446:
	s_or_b64 exec, exec, s[0:1]
	v_mul_f32_e32 v11, v54, v5
	s_waitcnt lgkmcnt(0)
	s_nop 1
	v_mov_b32_dpp v12, v11 quad_perm:[1,0,3,2] row_mask:0xf bank_mask:0xf
	s_and_saveexec_b64 s[0:1], s[2:3]
	s_cbranch_execz .LBB0_1448
	v_lshl_add_u64 v[14:15], v[8:9], 0, v[2:3]
	v_mov_b32_e32 v13, v245
	v_lshlrev_b32_e32 v14, 16, v13
	v_and_b32_e32 v13, 0xffff0000, v13
	v_mul_f32_e32 v11, v11, v14
	s_waitcnt lgkmcnt(0)
	v_mul_f32_e32 v12, v12, v13
	v_cvt_pk_bf16_f32 v11, v11, v12
	v_lshl_add_u64 v[12:13], v[6:7], 0, v[2:3]
	global_store_dword v[12:13], v11, off offset:64
.LBB0_1448:
	s_or_b64 exec, exec, s[0:1]
	v_mul_f32_e32 v11, v38, v5
	s_waitcnt lgkmcnt(0)
	s_nop 1
	v_mov_b32_dpp v12, v11 quad_perm:[1,0,3,2] row_mask:0xf bank_mask:0xf
	s_and_saveexec_b64 s[0:1], s[2:3]
	s_cbranch_execz .LBB0_1450
	v_lshl_add_u64 v[14:15], v[8:9], 0, v[2:3]
	v_mov_b32_e32 v13, v246
	v_lshlrev_b32_e32 v14, 16, v13
	v_and_b32_e32 v13, 0xffff0000, v13
	v_mul_f32_e32 v11, v11, v14
	s_waitcnt lgkmcnt(0)
	v_mul_f32_e32 v12, v12, v13
	v_cvt_pk_bf16_f32 v11, v11, v12
	v_lshl_add_u64 v[12:13], v[6:7], 0, v[2:3]
	global_store_dword v[12:13], v11, off offset:128
.LBB0_1450:
	s_or_b64 exec, exec, s[0:1]
	v_mul_f32_e32 v5, v22, v5
	s_nop 1
	v_mov_b32_dpp v11, v5 quad_perm:[1,0,3,2] row_mask:0xf bank_mask:0xf
	s_and_saveexec_b64 s[0:1], s[2:3]
	s_cbranch_execz .LBB0_1452
	v_lshl_add_u64 v[8:9], v[8:9], 0, v[2:3]
	v_lshl_add_u64 v[6:7], v[6:7], 0, v[2:3]
	v_mov_b32_e32 v8, v247
	v_lshlrev_b32_e32 v9, 16, v8
	v_and_b32_e32 v8, 0xffff0000, v8
	v_mul_f32_e32 v5, v5, v9
	s_waitcnt lgkmcnt(0)
	v_mul_f32_e32 v8, v11, v8
	v_cvt_pk_bf16_f32 v5, v5, v8
	global_store_dword v[6:7], v5, off offset:192
.LBB0_1452:
	s_or_b64 exec, exec, s[0:1]
	ds_read_b32 v5, v160 offset:36
	v_add_u32_e32 v6, 9, v4
	v_ashrrev_i32_e32 v7, 31, v6
	v_lshlrev_b64 v[8:9], 11, v[6:7]
	v_lshlrev_b64 v[6:7], 12, v[6:7]
	s_waitcnt lgkmcnt(0)
	v_rcp_f32_e32 v5, v5
	v_lshl_add_u64 v[8:9], s[6:7], 0, v[8:9]
	v_lshl_add_u64 v[6:7], s[8:9], 0, v[6:7]
	v_lshl_add_u64 v[242:243], v[8:9], 0, v[2:3]
	global_load_dword v244, v[242:243], off
	global_load_dword v245, v[242:243], off offset:64
	global_load_dword v246, v[242:243], off offset:128
	global_load_dword v247, v[242:243], off offset:192
	v_mul_f32_e32 v11, v71, v5
	s_nop 1
	v_mov_b32_dpp v12, v11 quad_perm:[1,0,3,2] row_mask:0xf bank_mask:0xf
	s_and_saveexec_b64 s[0:1], s[2:3]
	s_cbranch_execz .LBB0_1454
	v_lshl_add_u64 v[14:15], v[8:9], 0, v[2:3]
	s_waitcnt vmcnt(0)
	v_mov_b32_e32 v13, v244
	v_lshlrev_b32_e32 v14, 16, v13
	v_and_b32_e32 v13, 0xffff0000, v13
	v_mul_f32_e32 v11, v11, v14
	s_waitcnt lgkmcnt(0)
	v_mul_f32_e32 v12, v12, v13
	v_cvt_pk_bf16_f32 v11, v11, v12
	v_lshl_add_u64 v[12:13], v[6:7], 0, v[2:3]
	global_store_dword v[12:13], v11, off
.LBB0_1454:
	s_or_b64 exec, exec, s[0:1]
	v_mul_f32_e32 v11, v55, v5
	s_waitcnt lgkmcnt(0)
	s_nop 1
	v_mov_b32_dpp v12, v11 quad_perm:[1,0,3,2] row_mask:0xf bank_mask:0xf
	s_and_saveexec_b64 s[0:1], s[2:3]
	s_cbranch_execz .LBB0_1456
	v_lshl_add_u64 v[14:15], v[8:9], 0, v[2:3]
	v_mov_b32_e32 v13, v245
	v_lshlrev_b32_e32 v14, 16, v13
	v_and_b32_e32 v13, 0xffff0000, v13
	v_mul_f32_e32 v11, v11, v14
	s_waitcnt lgkmcnt(0)
	v_mul_f32_e32 v12, v12, v13
	v_cvt_pk_bf16_f32 v11, v11, v12
	v_lshl_add_u64 v[12:13], v[6:7], 0, v[2:3]
	global_store_dword v[12:13], v11, off offset:64
.LBB0_1456:
	s_or_b64 exec, exec, s[0:1]
	v_mul_f32_e32 v11, v39, v5
	s_waitcnt lgkmcnt(0)
	s_nop 1
	v_mov_b32_dpp v12, v11 quad_perm:[1,0,3,2] row_mask:0xf bank_mask:0xf
	s_and_saveexec_b64 s[0:1], s[2:3]
	s_cbranch_execz .LBB0_1458
	v_lshl_add_u64 v[14:15], v[8:9], 0, v[2:3]
	v_mov_b32_e32 v13, v246
	v_lshlrev_b32_e32 v14, 16, v13
	v_and_b32_e32 v13, 0xffff0000, v13
	v_mul_f32_e32 v11, v11, v14
	s_waitcnt lgkmcnt(0)
	v_mul_f32_e32 v12, v12, v13
	v_cvt_pk_bf16_f32 v11, v11, v12
	v_lshl_add_u64 v[12:13], v[6:7], 0, v[2:3]
	global_store_dword v[12:13], v11, off offset:128
.LBB0_1458:
	s_or_b64 exec, exec, s[0:1]
	v_mul_f32_e32 v5, v23, v5
	s_nop 1
	v_mov_b32_dpp v11, v5 quad_perm:[1,0,3,2] row_mask:0xf bank_mask:0xf
	s_and_saveexec_b64 s[0:1], s[2:3]
	s_cbranch_execz .LBB0_1460
	v_lshl_add_u64 v[8:9], v[8:9], 0, v[2:3]
	v_lshl_add_u64 v[6:7], v[6:7], 0, v[2:3]
	v_mov_b32_e32 v8, v247
	v_lshlrev_b32_e32 v9, 16, v8
	v_and_b32_e32 v8, 0xffff0000, v8
	v_mul_f32_e32 v5, v5, v9
	s_waitcnt lgkmcnt(0)
	v_mul_f32_e32 v8, v11, v8
	v_cvt_pk_bf16_f32 v5, v5, v8
	global_store_dword v[6:7], v5, off offset:192
; __device__ __forceinline__ unsigned cvt_pk_bf16(float lo, float hi) { unsigned r; asm volatile("v_cvt_pk_bf16_f32 %0, %1, %2" : "=v"(r) : "v"(lo), "v"(hi)); return r; }
; __device__ __forceinline__ float bf_lo(unsigned w) { return __uint_as_float(w << 16); }
; __device__ __forceinline__ float bf_hi(unsigned w) { return __uint_as_float(w & 0xffff0000u); }
; __device__ __forceinline__ int crow(int r, int hi) { return (r & 3) + 8 * (r >> 2) + 4 * hi; }
; template <int MODE> ...
;     ...
;     for (int r = 0; r < 16; ++r) { const int orow = qlo + crow(r, hi); const float rl = __builtin_amdgcn_rcpf(li_l[crow(r, hi)]);
; #pragma unroll
;         for (int d0 = 0; d0 < 4; ++d0) { float v = o[d0][r] * rl; float vn = __shfl_xor(v, 1);
;             if ((r32 & 1) == 0) { const int col = d0 * 32 + r32;
;                 if (MODE == 1) { const unsigned g = *(const unsigned*)(gate + (size_t)orow * 1024 + hoff + col); v *= bf_lo(g); vn *= bf_hi(g); }
;                 *(unsigned*)(Ob + (size_t)orow * DM + ocol0 + col) = cvt_pk_bf16(v, vn); } } }
.LBB0_1460:
	s_or_b64 exec, exec, s[0:1]
	ds_read_b32 v5, v160 offset:40
	v_add_u32_e32 v6, 10, v4
	v_ashrrev_i32_e32 v7, 31, v6
	v_lshlrev_b64 v[8:9], 11, v[6:7]
	v_lshlrev_b64 v[6:7], 12, v[6:7]
	s_waitcnt lgkmcnt(0)
	v_rcp_f32_e32 v5, v5
	v_lshl_add_u64 v[8:9], s[6:7], 0, v[8:9]
	v_lshl_add_u64 v[6:7], s[8:9], 0, v[6:7]
	v_lshl_add_u64 v[242:243], v[8:9], 0, v[2:3]
	global_load_dword v244, v[242:243], off
	global_load_dword v245, v[242:243], off offset:64
	global_load_dword v246, v[242:243], off offset:128
	global_load_dword v247, v[242:243], off offset:192
	v_mul_f32_e32 v11, v72, v5
	s_nop 1
	v_mov_b32_dpp v12, v11 quad_perm:[1,0,3,2] row_mask:0xf bank_mask:0xf
	s_and_saveexec_b64 s[0:1], s[2:3]
	s_cbranch_execz .LBB0_1462
	v_lshl_add_u64 v[14:15], v[8:9], 0, v[2:3]
	s_waitcnt vmcnt(0)
	v_mov_b32_e32 v13, v244
	v_lshlrev_b32_e32 v14, 16, v13
	v_and_b32_e32 v13, 0xffff0000, v13
	v_mul_f32_e32 v11, v11, v14
	s_waitcnt lgkmcnt(0)
	v_mul_f32_e32 v12, v12, v13
	v_cvt_pk_bf16_f32 v11, v11, v12
	v_lshl_add_u64 v[12:13], v[6:7], 0, v[2:3]
	global_store_dword v[12:13], v11, off
.LBB0_1462:
	s_or_b64 exec, exec, s[0:1]
	v_mul_f32_e32 v11, v56, v5
	s_waitcnt lgkmcnt(0)
	s_nop 1
	v_mov_b32_dpp v12, v11 quad_perm:[1,0,3,2] row_mask:0xf bank_mask:0xf
	s_and_saveexec_b64 s[0:1], s[2:3]
	s_cbranch_execz .LBB0_1464
	v_lshl_add_u64 v[14:15], v[8:9], 0, v[2:3]
	v_mov_b32_e32 v13, v245
	v_lshlrev_b32_e32 v14, 16, v13
	v_and_b32_e32 v13, 0xffff0000, v13
	v_mul_f32_e32 v11, v11, v14
	s_waitcnt lgkmcnt(0)
	v_mul_f32_e32 v12, v12, v13
	v_cvt_pk_bf16_f32 v11, v11, v12
	v_lshl_add_u64 v[12:13], v[6:7], 0, v[2:3]
	global_store_dword v[12:13], v11, off offset:64
.LBB0_1464:
	s_or_b64 exec, exec, s[0:1]
	v_mul_f32_e32 v11, v40, v5
	s_waitcnt lgkmcnt(0)
	s_nop 1
	v_mov_b32_dpp v12, v11 quad_perm:[1,0,3,2] row_mask:0xf bank_mask:0xf
	s_and_saveexec_b64 s[0:1], s[2:3]
	s_cbranch_execz .LBB0_1466
	v_lshl_add_u64 v[14:15], v[8:9], 0, v[2:3]
	v_mov_b32_e32 v13, v246
	v_lshlrev_b32_e32 v14, 16, v13
	v_and_b32_e32 v13, 0xffff0000, v13
	v_mul_f32_e32 v11, v11, v14
	s_waitcnt lgkmcnt(0)
	v_mul_f32_e32 v12, v12, v13
	v_cvt_pk_bf16_f32 v11, v11, v12
	v_lshl_add_u64 v[12:13], v[6:7], 0, v[2:3]
	global_store_dword v[12:13], v11, off offset:128
.LBB0_1466:
	s_or_b64 exec, exec, s[0:1]
	v_mul_f32_e32 v5, v24, v5
	s_nop 1
	v_mov_b32_dpp v11, v5 quad_perm:[1,0,3,2] row_mask:0xf bank_mask:0xf
	s_and_saveexec_b64 s[0:1], s[2:3]
	s_cbranch_execz .LBB0_1468
	v_lshl_add_u64 v[8:9], v[8:9], 0, v[2:3]
	v_lshl_add_u64 v[6:7], v[6:7], 0, v[2:3]
	v_mov_b32_e32 v8, v247
	v_lshlrev_b32_e32 v9, 16, v8
	v_and_b32_e32 v8, 0xffff0000, v8
	v_mul_f32_e32 v5, v5, v9
	s_waitcnt lgkmcnt(0)
	v_mul_f32_e32 v8, v11, v8
	v_cvt_pk_bf16_f32 v5, v5, v8
	global_store_dword v[6:7], v5, off offset:192
.LBB0_1468:
	s_or_b64 exec, exec, s[0:1]
	ds_read_b32 v5, v160 offset:44
	v_add_u32_e32 v6, 11, v4
	v_ashrrev_i32_e32 v7, 31, v6
	v_lshlrev_b64 v[8:9], 11, v[6:7]
	v_lshlrev_b64 v[6:7], 12, v[6:7]
	s_waitcnt lgkmcnt(0)
	v_rcp_f32_e32 v5, v5
	v_lshl_add_u64 v[8:9], s[6:7], 0, v[8:9]
	v_lshl_add_u64 v[6:7], s[8:9], 0, v[6:7]
	v_lshl_add_u64 v[242:243], v[8:9], 0, v[2:3]
	global_load_dword v244, v[242:243], off
	global_load_dword v245, v[242:243], off offset:64
	global_load_dword v246, v[242:243], off offset:128
	global_load_dword v247, v[242:243], off offset:192
	v_mul_f32_e32 v11, v73, v5
	s_nop 1
	v_mov_b32_dpp v12, v11 quad_perm:[1,0,3,2] row_mask:0xf bank_mask:0xf
	s_and_saveexec_b64 s[0:1], s[2:3]
	s_cbranch_execz .LBB0_1470
	v_lshl_add_u64 v[14:15], v[8:9], 0, v[2:3]
	s_waitcnt vmcnt(0)
	v_mov_b32_e32 v13, v244
	v_lshlrev_b32_e32 v14, 16, v13
	v_and_b32_e32 v13, 0xffff0000, v13
	v_mul_f32_e32 v11, v11, v14
	s_waitcnt lgkmcnt(0)
	v_mul_f32_e32 v12, v12, v13
	v_cvt_pk_bf16_f32 v11, v11, v12
	v_lshl_add_u64 v[12:13], v[6:7], 0, v[2:3]
	global_store_dword v[12:13], v11, off
.LBB0_1470:
	s_or_b64 exec, exec, s[0:1]
	v_mul_f32_e32 v11, v57, v5
	s_waitcnt lgkmcnt(0)
	s_nop 1
	v_mov_b32_dpp v12, v11 quad_perm:[1,0,3,2] row_mask:0xf bank_mask:0xf
	s_and_saveexec_b64 s[0:1], s[2:3]
	s_cbranch_execz .LBB0_1472
	v_lshl_add_u64 v[14:15], v[8:9], 0, v[2:3]
	v_mov_b32_e32 v13, v245
	v_lshlrev_b32_e32 v14, 16, v13
	v_and_b32_e32 v13, 0xffff0000, v13
	v_mul_f32_e32 v11, v11, v14
	s_waitcnt lgkmcnt(0)
	v_mul_f32_e32 v12, v12, v13
	v_cvt_pk_bf16_f32 v11, v11, v12
	v_lshl_add_u64 v[12:13], v[6:7], 0, v[2:3]
	global_store_dword v[12:13], v11, off offset:64
.LBB0_1472:
	s_or_b64 exec, exec, s[0:1]
	v_mul_f32_e32 v11, v41, v5
	s_waitcnt lgkmcnt(0)
	s_nop 1
	v_mov_b32_dpp v12, v11 quad_perm:[1,0,3,2] row_mask:0xf bank_mask:0xf
	s_and_saveexec_b64 s[0:1], s[2:3]
	s_cbranch_execz .LBB0_1474
	v_lshl_add_u64 v[14:15], v[8:9], 0, v[2:3]
	v_mov_b32_e32 v13, v246
	v_lshlrev_b32_e32 v14, 16, v13
	v_and_b32_e32 v13, 0xffff0000, v13
	v_mul_f32_e32 v11, v11, v14
	s_waitcnt lgkmcnt(0)
	v_mul_f32_e32 v12, v12, v13
	v_cvt_pk_bf16_f32 v11, v11, v12
	v_lshl_add_u64 v[12:13], v[6:7], 0, v[2:3]
	global_store_dword v[12:13], v11, off offset:128
.LBB0_1474:
	s_or_b64 exec, exec, s[0:1]
	v_mul_f32_e32 v5, v25, v5
	s_nop 1
	v_mov_b32_dpp v11, v5 quad_perm:[1,0,3,2] row_mask:0xf bank_mask:0xf
	s_and_saveexec_b64 s[0:1], s[2:3]
	s_cbranch_execz .LBB0_1476
	v_lshl_add_u64 v[8:9], v[8:9], 0, v[2:3]
	v_lshl_add_u64 v[6:7], v[6:7], 0, v[2:3]
	v_mov_b32_e32 v8, v247
	v_lshlrev_b32_e32 v9, 16, v8
	v_and_b32_e32 v8, 0xffff0000, v8
	v_mul_f32_e32 v5, v5, v9
	s_waitcnt lgkmcnt(0)
	v_mul_f32_e32 v8, v11, v8
	v_cvt_pk_bf16_f32 v5, v5, v8
	global_store_dword v[6:7], v5, off offset:192
; __device__ __forceinline__ unsigned cvt_pk_bf16(float lo, float hi) { unsigned r; asm volatile("v_cvt_pk_bf16_f32 %0, %1, %2" : "=v"(r) : "v"(lo), "v"(hi)); return r; }
; __device__ __forceinline__ float bf_lo(unsigned w) { return __uint_as_float(w << 16); }
; __device__ __forceinline__ float bf_hi(unsigned w) { return __uint_as_float(w & 0xffff0000u); }
; __device__ __forceinline__ int crow(int r, int hi) { return (r & 3) + 8 * (r >> 2) + 4 * hi; }
; template <int MODE> ...
;     ...
;     for (int r = 0; r < 16; ++r) { const int orow = qlo + crow(r, hi); const float rl = __builtin_amdgcn_rcpf(li_l[crow(r, hi)]);
; #pragma unroll
;         for (int d0 = 0; d0 < 4; ++d0) { float v = o[d0][r] * rl; float vn = __shfl_xor(v, 1);
;             if ((r32 & 1) == 0) { const int col = d0 * 32 + r32;
;                 if (MODE == 1) { const unsigned g = *(const unsigned*)(gate + (size_t)orow * 1024 + hoff + col); v *= bf_lo(g); vn *= bf_hi(g); }
;                 *(unsigned*)(Ob + (size_t)orow * DM + ocol0 + col) = cvt_pk_bf16(v, vn); } } }
.LBB0_1476:
	s_or_b64 exec, exec, s[0:1]
	ds_read_b32 v5, v160 offset:64
	v_add_u32_e32 v6, 16, v4
	v_ashrrev_i32_e32 v7, 31, v6
	v_lshlrev_b64 v[8:9], 11, v[6:7]
	v_lshlrev_b64 v[6:7], 12, v[6:7]
	s_waitcnt lgkmcnt(0)
	v_rcp_f32_e32 v5, v5
	v_lshl_add_u64 v[8:9], s[6:7], 0, v[8:9]
	v_lshl_add_u64 v[6:7], s[8:9], 0, v[6:7]
	v_lshl_add_u64 v[242:243], v[8:9], 0, v[2:3]
	global_load_dword v244, v[242:243], off
	global_load_dword v245, v[242:243], off offset:64
	global_load_dword v246, v[242:243], off offset:128
	global_load_dword v247, v[242:243], off offset:192
	v_mul_f32_e32 v11, v74, v5
	s_nop 1
	v_mov_b32_dpp v12, v11 quad_perm:[1,0,3,2] row_mask:0xf bank_mask:0xf
	s_and_saveexec_b64 s[0:1], s[2:3]
	s_cbranch_execz .LBB0_1478
	v_lshl_add_u64 v[14:15], v[8:9], 0, v[2:3]
	s_waitcnt vmcnt(0)
	v_mov_b32_e32 v13, v244
	v_lshlrev_b32_e32 v14, 16, v13
	v_and_b32_e32 v13, 0xffff0000, v13
	v_mul_f32_e32 v11, v11, v14
	s_waitcnt lgkmcnt(0)
	v_mul_f32_e32 v12, v12, v13
	v_cvt_pk_bf16_f32 v11, v11, v12
	v_lshl_add_u64 v[12:13], v[6:7], 0, v[2:3]
	global_store_dword v[12:13], v11, off
.LBB0_1478:
	s_or_b64 exec, exec, s[0:1]
	v_mul_f32_e32 v11, v58, v5
	s_waitcnt lgkmcnt(0)
	s_nop 1
	v_mov_b32_dpp v12, v11 quad_perm:[1,0,3,2] row_mask:0xf bank_mask:0xf
	s_and_saveexec_b64 s[0:1], s[2:3]
	s_cbranch_execz .LBB0_1480
	v_lshl_add_u64 v[14:15], v[8:9], 0, v[2:3]
	v_mov_b32_e32 v13, v245
	v_lshlrev_b32_e32 v14, 16, v13
	v_and_b32_e32 v13, 0xffff0000, v13
	v_mul_f32_e32 v11, v11, v14
	s_waitcnt lgkmcnt(0)
	v_mul_f32_e32 v12, v12, v13
	v_cvt_pk_bf16_f32 v11, v11, v12
	v_lshl_add_u64 v[12:13], v[6:7], 0, v[2:3]
	global_store_dword v[12:13], v11, off offset:64
.LBB0_1480:
	s_or_b64 exec, exec, s[0:1]
	v_mul_f32_e32 v11, v42, v5
	s_waitcnt lgkmcnt(0)
	s_nop 1
	v_mov_b32_dpp v12, v11 quad_perm:[1,0,3,2] row_mask:0xf bank_mask:0xf
	s_and_saveexec_b64 s[0:1], s[2:3]
	s_cbranch_execz .LBB0_1482
	v_lshl_add_u64 v[14:15], v[8:9], 0, v[2:3]
	v_mov_b32_e32 v13, v246
	v_lshlrev_b32_e32 v14, 16, v13
	v_and_b32_e32 v13, 0xffff0000, v13
	v_mul_f32_e32 v11, v11, v14
	s_waitcnt lgkmcnt(0)
	v_mul_f32_e32 v12, v12, v13
	v_cvt_pk_bf16_f32 v11, v11, v12
	v_lshl_add_u64 v[12:13], v[6:7], 0, v[2:3]
	global_store_dword v[12:13], v11, off offset:128
.LBB0_1482:
	s_or_b64 exec, exec, s[0:1]
	v_mul_f32_e32 v5, v26, v5
	s_nop 1
	v_mov_b32_dpp v11, v5 quad_perm:[1,0,3,2] row_mask:0xf bank_mask:0xf
	s_and_saveexec_b64 s[0:1], s[2:3]
	s_cbranch_execz .LBB0_1484
	v_lshl_add_u64 v[8:9], v[8:9], 0, v[2:3]
	v_lshl_add_u64 v[6:7], v[6:7], 0, v[2:3]
	v_mov_b32_e32 v8, v247
	v_lshlrev_b32_e32 v9, 16, v8
	v_and_b32_e32 v8, 0xffff0000, v8
	v_mul_f32_e32 v5, v5, v9
	s_waitcnt lgkmcnt(0)
	v_mul_f32_e32 v8, v11, v8
	v_cvt_pk_bf16_f32 v5, v5, v8
	global_store_dword v[6:7], v5, off offset:192
.LBB0_1484:
	s_or_b64 exec, exec, s[0:1]
	ds_read_b32 v5, v160 offset:68
	v_add_u32_e32 v6, 17, v4
	v_ashrrev_i32_e32 v7, 31, v6
	v_lshlrev_b64 v[8:9], 11, v[6:7]
	v_lshlrev_b64 v[6:7], 12, v[6:7]
	s_waitcnt lgkmcnt(0)
	v_rcp_f32_e32 v5, v5
	v_lshl_add_u64 v[8:9], s[6:7], 0, v[8:9]
	v_lshl_add_u64 v[6:7], s[8:9], 0, v[6:7]
	v_lshl_add_u64 v[242:243], v[8:9], 0, v[2:3]
	global_load_dword v244, v[242:243], off
	global_load_dword v245, v[242:243], off offset:64
	global_load_dword v246, v[242:243], off offset:128
	global_load_dword v247, v[242:243], off offset:192
	v_mul_f32_e32 v11, v75, v5
	s_nop 1
	v_mov_b32_dpp v12, v11 quad_perm:[1,0,3,2] row_mask:0xf bank_mask:0xf
	s_and_saveexec_b64 s[0:1], s[2:3]
	s_cbranch_execz .LBB0_1486
	v_lshl_add_u64 v[14:15], v[8:9], 0, v[2:3]
	s_waitcnt vmcnt(0)
	v_mov_b32_e32 v13, v244
	v_lshlrev_b32_e32 v14, 16, v13
	v_and_b32_e32 v13, 0xffff0000, v13
	v_mul_f32_e32 v11, v11, v14
	s_waitcnt lgkmcnt(0)
	v_mul_f32_e32 v12, v12, v13
	v_cvt_pk_bf16_f32 v11, v11, v12
	v_lshl_add_u64 v[12:13], v[6:7], 0, v[2:3]
	global_store_dword v[12:13], v11, off
.LBB0_1486:
	s_or_b64 exec, exec, s[0:1]
	v_mul_f32_e32 v11, v59, v5
	s_waitcnt lgkmcnt(0)
	s_nop 1
	v_mov_b32_dpp v12, v11 quad_perm:[1,0,3,2] row_mask:0xf bank_mask:0xf
	s_and_saveexec_b64 s[0:1], s[2:3]
	s_cbranch_execz .LBB0_1488
	v_lshl_add_u64 v[14:15], v[8:9], 0, v[2:3]
	v_mov_b32_e32 v13, v245
	v_lshlrev_b32_e32 v14, 16, v13
	v_and_b32_e32 v13, 0xffff0000, v13
	v_mul_f32_e32 v11, v11, v14
	s_waitcnt lgkmcnt(0)
	v_mul_f32_e32 v12, v12, v13
	v_cvt_pk_bf16_f32 v11, v11, v12
	v_lshl_add_u64 v[12:13], v[6:7], 0, v[2:3]
	global_store_dword v[12:13], v11, off offset:64
.LBB0_1488:
	s_or_b64 exec, exec, s[0:1]
	v_mul_f32_e32 v11, v43, v5
	s_waitcnt lgkmcnt(0)
	s_nop 1
	v_mov_b32_dpp v12, v11 quad_perm:[1,0,3,2] row_mask:0xf bank_mask:0xf
	s_and_saveexec_b64 s[0:1], s[2:3]
	s_cbranch_execz .LBB0_1490
	v_lshl_add_u64 v[14:15], v[8:9], 0, v[2:3]
	v_mov_b32_e32 v13, v246
	v_lshlrev_b32_e32 v14, 16, v13
	v_and_b32_e32 v13, 0xffff0000, v13
	v_mul_f32_e32 v11, v11, v14
	s_waitcnt lgkmcnt(0)
	v_mul_f32_e32 v12, v12, v13
	v_cvt_pk_bf16_f32 v11, v11, v12
	v_lshl_add_u64 v[12:13], v[6:7], 0, v[2:3]
	global_store_dword v[12:13], v11, off offset:128
.LBB0_1490:
	s_or_b64 exec, exec, s[0:1]
	v_mul_f32_e32 v5, v27, v5
	s_nop 1
	v_mov_b32_dpp v11, v5 quad_perm:[1,0,3,2] row_mask:0xf bank_mask:0xf
	s_and_saveexec_b64 s[0:1], s[2:3]
	s_cbranch_execz .LBB0_1492
	v_lshl_add_u64 v[8:9], v[8:9], 0, v[2:3]
	v_lshl_add_u64 v[6:7], v[6:7], 0, v[2:3]
	v_mov_b32_e32 v8, v247
	v_lshlrev_b32_e32 v9, 16, v8
	v_and_b32_e32 v8, 0xffff0000, v8
	v_mul_f32_e32 v5, v5, v9
	s_waitcnt lgkmcnt(0)
	v_mul_f32_e32 v8, v11, v8
	v_cvt_pk_bf16_f32 v5, v5, v8
	global_store_dword v[6:7], v5, off offset:192
; __device__ __forceinline__ unsigned cvt_pk_bf16(float lo, float hi) { unsigned r; asm volatile("v_cvt_pk_bf16_f32 %0, %1, %2" : "=v"(r) : "v"(lo), "v"(hi)); return r; }
; __device__ __forceinline__ float bf_lo(unsigned w) { return __uint_as_float(w << 16); }
; __device__ __forceinline__ float bf_hi(unsigned w) { return __uint_as_float(w & 0xffff0000u); }
; __device__ __forceinline__ int crow(int r, int hi) { return (r & 3) + 8 * (r >> 2) + 4 * hi; }
; template <int MODE> ...
;     ...
;     for (int r = 0; r < 16; ++r) { const int orow = qlo + crow(r, hi); const float rl = __builtin_amdgcn_rcpf(li_l[crow(r, hi)]);
; #pragma unroll
;         for (int d0 = 0; d0 < 4; ++d0) { float v = o[d0][r] * rl; float vn = __shfl_xor(v, 1);
;             if ((r32 & 1) == 0) { const int col = d0 * 32 + r32;
;                 if (MODE == 1) { const unsigned g = *(const unsigned*)(gate + (size_t)orow * 1024 + hoff + col); v *= bf_lo(g); vn *= bf_hi(g); }
;                 *(unsigned*)(Ob + (size_t)orow * DM + ocol0 + col) = cvt_pk_bf16(v, vn); } } }
.LBB0_1492:
	s_or_b64 exec, exec, s[0:1]
	ds_read_b32 v5, v160 offset:72
	v_add_u32_e32 v6, 18, v4
	v_ashrrev_i32_e32 v7, 31, v6
	v_lshlrev_b64 v[8:9], 11, v[6:7]
	v_lshlrev_b64 v[6:7], 12, v[6:7]
	s_waitcnt lgkmcnt(0)
	v_rcp_f32_e32 v5, v5
	v_lshl_add_u64 v[8:9], s[6:7], 0, v[8:9]
	v_lshl_add_u64 v[6:7], s[8:9], 0, v[6:7]
	v_lshl_add_u64 v[242:243], v[8:9], 0, v[2:3]
	global_load_dword v244, v[242:243], off
	global_load_dword v245, v[242:243], off offset:64
	global_load_dword v246, v[242:243], off offset:128
	global_load_dword v247, v[242:243], off offset:192
	v_mul_f32_e32 v11, v76, v5
	s_nop 1
	v_mov_b32_dpp v12, v11 quad_perm:[1,0,3,2] row_mask:0xf bank_mask:0xf
	s_and_saveexec_b64 s[0:1], s[2:3]
	s_cbranch_execz .LBB0_1494
	v_lshl_add_u64 v[14:15], v[8:9], 0, v[2:3]
	s_waitcnt vmcnt(0)
	v_mov_b32_e32 v13, v244
	v_lshlrev_b32_e32 v14, 16, v13
	v_and_b32_e32 v13, 0xffff0000, v13
	v_mul_f32_e32 v11, v11, v14
	s_waitcnt lgkmcnt(0)
	v_mul_f32_e32 v12, v12, v13
	v_cvt_pk_bf16_f32 v11, v11, v12
	v_lshl_add_u64 v[12:13], v[6:7], 0, v[2:3]
	global_store_dword v[12:13], v11, off
.LBB0_1494:
	s_or_b64 exec, exec, s[0:1]
	v_mul_f32_e32 v11, v60, v5
	s_waitcnt lgkmcnt(0)
	s_nop 1
	v_mov_b32_dpp v12, v11 quad_perm:[1,0,3,2] row_mask:0xf bank_mask:0xf
	s_and_saveexec_b64 s[0:1], s[2:3]
	s_cbranch_execz .LBB0_1496
	v_lshl_add_u64 v[14:15], v[8:9], 0, v[2:3]
	v_mov_b32_e32 v13, v245
	v_lshlrev_b32_e32 v14, 16, v13
	v_and_b32_e32 v13, 0xffff0000, v13
	v_mul_f32_e32 v11, v11, v14
	s_waitcnt lgkmcnt(0)
	v_mul_f32_e32 v12, v12, v13
	v_cvt_pk_bf16_f32 v11, v11, v12
	v_lshl_add_u64 v[12:13], v[6:7], 0, v[2:3]
	global_store_dword v[12:13], v11, off offset:64
.LBB0_1496:
	s_or_b64 exec, exec, s[0:1]
	v_mul_f32_e32 v11, v44, v5
	s_waitcnt lgkmcnt(0)
	s_nop 1
	v_mov_b32_dpp v12, v11 quad_perm:[1,0,3,2] row_mask:0xf bank_mask:0xf
	s_and_saveexec_b64 s[0:1], s[2:3]
	s_cbranch_execz .LBB0_1498
	v_lshl_add_u64 v[14:15], v[8:9], 0, v[2:3]
	v_mov_b32_e32 v13, v246
	v_lshlrev_b32_e32 v14, 16, v13
	v_and_b32_e32 v13, 0xffff0000, v13
	v_mul_f32_e32 v11, v11, v14
	s_waitcnt lgkmcnt(0)
	v_mul_f32_e32 v12, v12, v13
	v_cvt_pk_bf16_f32 v11, v11, v12
	v_lshl_add_u64 v[12:13], v[6:7], 0, v[2:3]
	global_store_dword v[12:13], v11, off offset:128
.LBB0_1498:
	s_or_b64 exec, exec, s[0:1]
	v_mul_f32_e32 v5, v28, v5
	s_nop 1
	v_mov_b32_dpp v11, v5 quad_perm:[1,0,3,2] row_mask:0xf bank_mask:0xf
	s_and_saveexec_b64 s[0:1], s[2:3]
	s_cbranch_execz .LBB0_1500
	v_lshl_add_u64 v[8:9], v[8:9], 0, v[2:3]
	v_lshl_add_u64 v[6:7], v[6:7], 0, v[2:3]
	v_mov_b32_e32 v8, v247
	v_lshlrev_b32_e32 v9, 16, v8
	v_and_b32_e32 v8, 0xffff0000, v8
	v_mul_f32_e32 v5, v5, v9
	s_waitcnt lgkmcnt(0)
	v_mul_f32_e32 v8, v11, v8
	v_cvt_pk_bf16_f32 v5, v5, v8
	global_store_dword v[6:7], v5, off offset:192
.LBB0_1500:
	s_or_b64 exec, exec, s[0:1]
	ds_read_b32 v5, v160 offset:76
	v_add_u32_e32 v6, 19, v4
	v_ashrrev_i32_e32 v7, 31, v6
	v_lshlrev_b64 v[8:9], 11, v[6:7]
	v_lshlrev_b64 v[6:7], 12, v[6:7]
	s_waitcnt lgkmcnt(0)
	v_rcp_f32_e32 v5, v5
	v_lshl_add_u64 v[8:9], s[6:7], 0, v[8:9]
	v_lshl_add_u64 v[6:7], s[8:9], 0, v[6:7]
	v_lshl_add_u64 v[242:243], v[8:9], 0, v[2:3]
	global_load_dword v244, v[242:243], off
	global_load_dword v245, v[242:243], off offset:64
	global_load_dword v246, v[242:243], off offset:128
	global_load_dword v247, v[242:243], off offset:192
	v_mul_f32_e32 v11, v77, v5
	s_nop 1
	v_mov_b32_dpp v12, v11 quad_perm:[1,0,3,2] row_mask:0xf bank_mask:0xf
	s_and_saveexec_b64 s[0:1], s[2:3]
	s_cbranch_execz .LBB0_1502
	v_lshl_add_u64 v[14:15], v[8:9], 0, v[2:3]
	s_waitcnt vmcnt(0)
	v_mov_b32_e32 v13, v244
	v_lshlrev_b32_e32 v14, 16, v13
	v_and_b32_e32 v13, 0xffff0000, v13
	v_mul_f32_e32 v11, v11, v14
	s_waitcnt lgkmcnt(0)
	v_mul_f32_e32 v12, v12, v13
	v_cvt_pk_bf16_f32 v11, v11, v12
	v_lshl_add_u64 v[12:13], v[6:7], 0, v[2:3]
	global_store_dword v[12:13], v11, off
.LBB0_1502:
	s_or_b64 exec, exec, s[0:1]
	v_mul_f32_e32 v11, v61, v5
	s_waitcnt lgkmcnt(0)
	s_nop 1
	v_mov_b32_dpp v12, v11 quad_perm:[1,0,3,2] row_mask:0xf bank_mask:0xf
	s_and_saveexec_b64 s[0:1], s[2:3]
	s_cbranch_execz .LBB0_1504
	v_lshl_add_u64 v[14:15], v[8:9], 0, v[2:3]
	v_mov_b32_e32 v13, v245
	v_lshlrev_b32_e32 v14, 16, v13
	v_and_b32_e32 v13, 0xffff0000, v13
	v_mul_f32_e32 v11, v11, v14
	s_waitcnt lgkmcnt(0)
	v_mul_f32_e32 v12, v12, v13
	v_cvt_pk_bf16_f32 v11, v11, v12
	v_lshl_add_u64 v[12:13], v[6:7], 0, v[2:3]
	global_store_dword v[12:13], v11, off offset:64
.LBB0_1504:
	s_or_b64 exec, exec, s[0:1]
	v_mul_f32_e32 v11, v45, v5
	s_waitcnt lgkmcnt(0)
	s_nop 1
	v_mov_b32_dpp v12, v11 quad_perm:[1,0,3,2] row_mask:0xf bank_mask:0xf
	s_and_saveexec_b64 s[0:1], s[2:3]
	s_cbranch_execz .LBB0_1506
	v_lshl_add_u64 v[14:15], v[8:9], 0, v[2:3]
	v_mov_b32_e32 v13, v246
	v_lshlrev_b32_e32 v14, 16, v13
	v_and_b32_e32 v13, 0xffff0000, v13
	v_mul_f32_e32 v11, v11, v14
	s_waitcnt lgkmcnt(0)
	v_mul_f32_e32 v12, v12, v13
	v_cvt_pk_bf16_f32 v11, v11, v12
	v_lshl_add_u64 v[12:13], v[6:7], 0, v[2:3]
	global_store_dword v[12:13], v11, off offset:128
.LBB0_1506:
	s_or_b64 exec, exec, s[0:1]
	v_mul_f32_e32 v5, v29, v5
	s_nop 1
	v_mov_b32_dpp v11, v5 quad_perm:[1,0,3,2] row_mask:0xf bank_mask:0xf
	s_and_saveexec_b64 s[0:1], s[2:3]
	s_cbranch_execz .LBB0_1508
	v_lshl_add_u64 v[8:9], v[8:9], 0, v[2:3]
	v_lshl_add_u64 v[6:7], v[6:7], 0, v[2:3]
	v_mov_b32_e32 v8, v247
	v_lshlrev_b32_e32 v9, 16, v8
	v_and_b32_e32 v8, 0xffff0000, v8
	v_mul_f32_e32 v5, v5, v9
	s_waitcnt lgkmcnt(0)
	v_mul_f32_e32 v8, v11, v8
	v_cvt_pk_bf16_f32 v5, v5, v8
	global_store_dword v[6:7], v5, off offset:192
; __device__ __forceinline__ unsigned cvt_pk_bf16(float lo, float hi) { unsigned r; asm volatile("v_cvt_pk_bf16_f32 %0, %1, %2" : "=v"(r) : "v"(lo), "v"(hi)); return r; }
; __device__ __forceinline__ float bf_lo(unsigned w) { return __uint_as_float(w << 16); }
; __device__ __forceinline__ float bf_hi(unsigned w) { return __uint_as_float(w & 0xffff0000u); }
; __device__ __forceinline__ int crow(int r, int hi) { return (r & 3) + 8 * (r >> 2) + 4 * hi; }
; template <int MODE> ...
;     ...
;     for (int r = 0; r < 16; ++r) { const int orow = qlo + crow(r, hi); const float rl = __builtin_amdgcn_rcpf(li_l[crow(r, hi)]);
; #pragma unroll
;         for (int d0 = 0; d0 < 4; ++d0) { float v = o[d0][r] * rl; float vn = __shfl_xor(v, 1);
;             if ((r32 & 1) == 0) { const int col = d0 * 32 + r32;
;                 if (MODE == 1) { const unsigned g = *(const unsigned*)(gate + (size_t)orow * 1024 + hoff + col); v *= bf_lo(g); vn *= bf_hi(g); }
;                 *(unsigned*)(Ob + (size_t)orow * DM + ocol0 + col) = cvt_pk_bf16(v, vn); } } }
.LBB0_1508:
	s_or_b64 exec, exec, s[0:1]
	ds_read_b32 v5, v160 offset:96
	v_add_u32_e32 v6, 24, v4
	v_ashrrev_i32_e32 v7, 31, v6
	v_lshlrev_b64 v[8:9], 11, v[6:7]
	v_lshlrev_b64 v[6:7], 12, v[6:7]
	s_waitcnt lgkmcnt(0)
	v_rcp_f32_e32 v5, v5
	v_lshl_add_u64 v[8:9], s[6:7], 0, v[8:9]
	v_lshl_add_u64 v[6:7], s[8:9], 0, v[6:7]
	v_lshl_add_u64 v[242:243], v[8:9], 0, v[2:3]
	global_load_dword v244, v[242:243], off
	global_load_dword v245, v[242:243], off offset:64
	global_load_dword v246, v[242:243], off offset:128
	global_load_dword v247, v[242:243], off offset:192
	v_mul_f32_e32 v11, v78, v5
	s_nop 1
	v_mov_b32_dpp v12, v11 quad_perm:[1,0,3,2] row_mask:0xf bank_mask:0xf
	s_and_saveexec_b64 s[0:1], s[2:3]
	s_cbranch_execz .LBB0_1510
	v_lshl_add_u64 v[14:15], v[8:9], 0, v[2:3]
	s_waitcnt vmcnt(0)
	v_mov_b32_e32 v13, v244
	v_lshlrev_b32_e32 v14, 16, v13
	v_and_b32_e32 v13, 0xffff0000, v13
	v_mul_f32_e32 v11, v11, v14
	s_waitcnt lgkmcnt(0)
	v_mul_f32_e32 v12, v12, v13
	v_cvt_pk_bf16_f32 v11, v11, v12
	v_lshl_add_u64 v[12:13], v[6:7], 0, v[2:3]
	global_store_dword v[12:13], v11, off
.LBB0_1510:
	s_or_b64 exec, exec, s[0:1]
	v_mul_f32_e32 v11, v62, v5
	s_waitcnt lgkmcnt(0)
	s_nop 1
	v_mov_b32_dpp v12, v11 quad_perm:[1,0,3,2] row_mask:0xf bank_mask:0xf
	s_and_saveexec_b64 s[0:1], s[2:3]
	s_cbranch_execz .LBB0_1512
	v_lshl_add_u64 v[14:15], v[8:9], 0, v[2:3]
	v_mov_b32_e32 v13, v245
	v_lshlrev_b32_e32 v14, 16, v13
	v_and_b32_e32 v13, 0xffff0000, v13
	v_mul_f32_e32 v11, v11, v14
	s_waitcnt lgkmcnt(0)
	v_mul_f32_e32 v12, v12, v13
	v_cvt_pk_bf16_f32 v11, v11, v12
	v_lshl_add_u64 v[12:13], v[6:7], 0, v[2:3]
	global_store_dword v[12:13], v11, off offset:64
.LBB0_1512:
	s_or_b64 exec, exec, s[0:1]
	v_mul_f32_e32 v11, v46, v5
	s_waitcnt lgkmcnt(0)
	s_nop 1
	v_mov_b32_dpp v12, v11 quad_perm:[1,0,3,2] row_mask:0xf bank_mask:0xf
	s_and_saveexec_b64 s[0:1], s[2:3]
	s_cbranch_execz .LBB0_1514
	v_lshl_add_u64 v[14:15], v[8:9], 0, v[2:3]
	v_mov_b32_e32 v13, v246
	v_lshlrev_b32_e32 v14, 16, v13
	v_and_b32_e32 v13, 0xffff0000, v13
	v_mul_f32_e32 v11, v11, v14
	s_waitcnt lgkmcnt(0)
	v_mul_f32_e32 v12, v12, v13
	v_cvt_pk_bf16_f32 v11, v11, v12
	v_lshl_add_u64 v[12:13], v[6:7], 0, v[2:3]
	global_store_dword v[12:13], v11, off offset:128
.LBB0_1514:
	s_or_b64 exec, exec, s[0:1]
	v_mul_f32_e32 v5, v30, v5
	s_nop 1
	v_mov_b32_dpp v11, v5 quad_perm:[1,0,3,2] row_mask:0xf bank_mask:0xf
	s_and_saveexec_b64 s[0:1], s[2:3]
	s_cbranch_execz .LBB0_1516
	v_lshl_add_u64 v[8:9], v[8:9], 0, v[2:3]
	v_lshl_add_u64 v[6:7], v[6:7], 0, v[2:3]
	v_mov_b32_e32 v8, v247
	v_lshlrev_b32_e32 v9, 16, v8
	v_and_b32_e32 v8, 0xffff0000, v8
	v_mul_f32_e32 v5, v5, v9
	s_waitcnt lgkmcnt(0)
	v_mul_f32_e32 v8, v11, v8
	v_cvt_pk_bf16_f32 v5, v5, v8
	global_store_dword v[6:7], v5, off offset:192
.LBB0_1516:
	s_or_b64 exec, exec, s[0:1]
	ds_read_b32 v5, v160 offset:100
	v_add_u32_e32 v6, 25, v4
	v_ashrrev_i32_e32 v7, 31, v6
	v_lshlrev_b64 v[8:9], 11, v[6:7]
	v_lshlrev_b64 v[6:7], 12, v[6:7]
	s_waitcnt lgkmcnt(0)
	v_rcp_f32_e32 v5, v5
	v_lshl_add_u64 v[8:9], s[6:7], 0, v[8:9]
	v_lshl_add_u64 v[6:7], s[8:9], 0, v[6:7]
	v_lshl_add_u64 v[242:243], v[8:9], 0, v[2:3]
	global_load_dword v244, v[242:243], off
	global_load_dword v245, v[242:243], off offset:64
	global_load_dword v246, v[242:243], off offset:128
	global_load_dword v247, v[242:243], off offset:192
	v_mul_f32_e32 v11, v79, v5
	s_nop 1
	v_mov_b32_dpp v12, v11 quad_perm:[1,0,3,2] row_mask:0xf bank_mask:0xf
	s_and_saveexec_b64 s[0:1], s[2:3]
	s_cbranch_execz .LBB0_1518
	v_lshl_add_u64 v[14:15], v[8:9], 0, v[2:3]
	s_waitcnt vmcnt(0)
	v_mov_b32_e32 v13, v244
	v_lshlrev_b32_e32 v14, 16, v13
	v_and_b32_e32 v13, 0xffff0000, v13
	v_mul_f32_e32 v11, v11, v14
	s_waitcnt lgkmcnt(0)
	v_mul_f32_e32 v12, v12, v13
	v_cvt_pk_bf16_f32 v11, v11, v12
	v_lshl_add_u64 v[12:13], v[6:7], 0, v[2:3]
	global_store_dword v[12:13], v11, off
.LBB0_1518:
	s_or_b64 exec, exec, s[0:1]
	v_mul_f32_e32 v11, v63, v5
	s_waitcnt lgkmcnt(0)
	s_nop 1
	v_mov_b32_dpp v12, v11 quad_perm:[1,0,3,2] row_mask:0xf bank_mask:0xf
	s_and_saveexec_b64 s[0:1], s[2:3]
	s_cbranch_execz .LBB0_1520
	v_lshl_add_u64 v[14:15], v[8:9], 0, v[2:3]
	v_mov_b32_e32 v13, v245
	v_lshlrev_b32_e32 v14, 16, v13
	v_and_b32_e32 v13, 0xffff0000, v13
	v_mul_f32_e32 v11, v11, v14
	s_waitcnt lgkmcnt(0)
	v_mul_f32_e32 v12, v12, v13
	v_cvt_pk_bf16_f32 v11, v11, v12
	v_lshl_add_u64 v[12:13], v[6:7], 0, v[2:3]
	global_store_dword v[12:13], v11, off offset:64
.LBB0_1520:
	s_or_b64 exec, exec, s[0:1]
	v_mul_f32_e32 v11, v47, v5
	s_waitcnt lgkmcnt(0)
	s_nop 1
	v_mov_b32_dpp v12, v11 quad_perm:[1,0,3,2] row_mask:0xf bank_mask:0xf
	s_and_saveexec_b64 s[0:1], s[2:3]
	s_cbranch_execz .LBB0_1522
	v_lshl_add_u64 v[14:15], v[8:9], 0, v[2:3]
	v_mov_b32_e32 v13, v246
	v_lshlrev_b32_e32 v14, 16, v13
	v_and_b32_e32 v13, 0xffff0000, v13
	v_mul_f32_e32 v11, v11, v14
	s_waitcnt lgkmcnt(0)
	v_mul_f32_e32 v12, v12, v13
	v_cvt_pk_bf16_f32 v11, v11, v12
	v_lshl_add_u64 v[12:13], v[6:7], 0, v[2:3]
	global_store_dword v[12:13], v11, off offset:128
.LBB0_1522:
	s_or_b64 exec, exec, s[0:1]
	v_mul_f32_e32 v5, v31, v5
	s_nop 1
	v_mov_b32_dpp v11, v5 quad_perm:[1,0,3,2] row_mask:0xf bank_mask:0xf
	s_and_saveexec_b64 s[0:1], s[2:3]
	s_cbranch_execz .LBB0_1524
	v_lshl_add_u64 v[8:9], v[8:9], 0, v[2:3]
	v_lshl_add_u64 v[6:7], v[6:7], 0, v[2:3]
	v_mov_b32_e32 v8, v247
	v_lshlrev_b32_e32 v9, 16, v8
	v_and_b32_e32 v8, 0xffff0000, v8
	v_mul_f32_e32 v5, v5, v9
	s_waitcnt lgkmcnt(0)
	v_mul_f32_e32 v8, v11, v8
	v_cvt_pk_bf16_f32 v5, v5, v8
	global_store_dword v[6:7], v5, off offset:192
; __device__ __forceinline__ unsigned cvt_pk_bf16(float lo, float hi) { unsigned r; asm volatile("v_cvt_pk_bf16_f32 %0, %1, %2" : "=v"(r) : "v"(lo), "v"(hi)); return r; }
; __device__ __forceinline__ float bf_lo(unsigned w) { return __uint_as_float(w << 16); }
; __device__ __forceinline__ float bf_hi(unsigned w) { return __uint_as_float(w & 0xffff0000u); }
; __device__ __forceinline__ int crow(int r, int hi) { return (r & 3) + 8 * (r >> 2) + 4 * hi; }
; template <int MODE> ...
;     ...
;     for (int r = 0; r < 16; ++r) { const int orow = qlo + crow(r, hi); const float rl = __builtin_amdgcn_rcpf(li_l[crow(r, hi)]);
; #pragma unroll
;         for (int d0 = 0; d0 < 4; ++d0) { float v = o[d0][r] * rl; float vn = __shfl_xor(v, 1);
;             if ((r32 & 1) == 0) { const int col = d0 * 32 + r32;
;                 if (MODE == 1) { const unsigned g = *(const unsigned*)(gate + (size_t)orow * 1024 + hoff + col); v *= bf_lo(g); vn *= bf_hi(g); }
;                 *(unsigned*)(Ob + (size_t)orow * DM + ocol0 + col) = cvt_pk_bf16(v, vn); } } }
.LBB0_1524:
	s_or_b64 exec, exec, s[0:1]
	ds_read_b32 v5, v160 offset:104
	v_add_u32_e32 v6, 26, v4
	v_ashrrev_i32_e32 v7, 31, v6
	v_lshlrev_b64 v[8:9], 11, v[6:7]
	v_lshlrev_b64 v[6:7], 12, v[6:7]
	s_waitcnt lgkmcnt(0)
	v_rcp_f32_e32 v5, v5
	v_lshl_add_u64 v[8:9], s[6:7], 0, v[8:9]
	v_lshl_add_u64 v[6:7], s[8:9], 0, v[6:7]
	v_lshl_add_u64 v[242:243], v[8:9], 0, v[2:3]
	global_load_dword v244, v[242:243], off
	global_load_dword v245, v[242:243], off offset:64
	global_load_dword v246, v[242:243], off offset:128
	global_load_dword v247, v[242:243], off offset:192
	v_mul_f32_e32 v11, v80, v5
	s_nop 1
	v_mov_b32_dpp v12, v11 quad_perm:[1,0,3,2] row_mask:0xf bank_mask:0xf
	s_and_saveexec_b64 s[0:1], s[2:3]
	s_cbranch_execz .LBB0_1526
	v_lshl_add_u64 v[14:15], v[8:9], 0, v[2:3]
	s_waitcnt vmcnt(0)
	v_mov_b32_e32 v13, v244
	v_lshlrev_b32_e32 v14, 16, v13
	v_and_b32_e32 v13, 0xffff0000, v13
	v_mul_f32_e32 v11, v11, v14
	s_waitcnt lgkmcnt(0)
	v_mul_f32_e32 v12, v12, v13
	v_cvt_pk_bf16_f32 v11, v11, v12
	v_lshl_add_u64 v[12:13], v[6:7], 0, v[2:3]
	global_store_dword v[12:13], v11, off
.LBB0_1526:
	s_or_b64 exec, exec, s[0:1]
	v_mul_f32_e32 v11, v64, v5
	s_waitcnt lgkmcnt(0)
	s_nop 1
	v_mov_b32_dpp v12, v11 quad_perm:[1,0,3,2] row_mask:0xf bank_mask:0xf
	s_and_saveexec_b64 s[0:1], s[2:3]
	s_cbranch_execz .LBB0_1528
	v_lshl_add_u64 v[14:15], v[8:9], 0, v[2:3]
	v_mov_b32_e32 v13, v245
	v_lshlrev_b32_e32 v14, 16, v13
	v_and_b32_e32 v13, 0xffff0000, v13
	v_mul_f32_e32 v11, v11, v14
	s_waitcnt lgkmcnt(0)
	v_mul_f32_e32 v12, v12, v13
	v_cvt_pk_bf16_f32 v11, v11, v12
	v_lshl_add_u64 v[12:13], v[6:7], 0, v[2:3]
	global_store_dword v[12:13], v11, off offset:64
.LBB0_1528:
	s_or_b64 exec, exec, s[0:1]
	v_mul_f32_e32 v11, v48, v5
	s_waitcnt lgkmcnt(0)
	s_nop 1
	v_mov_b32_dpp v12, v11 quad_perm:[1,0,3,2] row_mask:0xf bank_mask:0xf
	s_and_saveexec_b64 s[0:1], s[2:3]
	s_cbranch_execz .LBB0_1530
	v_lshl_add_u64 v[14:15], v[8:9], 0, v[2:3]
	v_mov_b32_e32 v13, v246
	v_lshlrev_b32_e32 v14, 16, v13
	v_and_b32_e32 v13, 0xffff0000, v13
	v_mul_f32_e32 v11, v11, v14
	s_waitcnt lgkmcnt(0)
	v_mul_f32_e32 v12, v12, v13
	v_cvt_pk_bf16_f32 v11, v11, v12
	v_lshl_add_u64 v[12:13], v[6:7], 0, v[2:3]
	global_store_dword v[12:13], v11, off offset:128
.LBB0_1530:
	s_or_b64 exec, exec, s[0:1]
	v_mul_f32_e32 v5, v32, v5
	s_nop 1
	v_mov_b32_dpp v11, v5 quad_perm:[1,0,3,2] row_mask:0xf bank_mask:0xf
	s_and_saveexec_b64 s[0:1], s[2:3]
	s_cbranch_execz .LBB0_1532
	v_lshl_add_u64 v[8:9], v[8:9], 0, v[2:3]
	v_lshl_add_u64 v[6:7], v[6:7], 0, v[2:3]
	v_mov_b32_e32 v8, v247
	v_lshlrev_b32_e32 v9, 16, v8
	v_and_b32_e32 v8, 0xffff0000, v8
	v_mul_f32_e32 v5, v5, v9
	s_waitcnt lgkmcnt(0)
	v_mul_f32_e32 v8, v11, v8
	v_cvt_pk_bf16_f32 v5, v5, v8
	global_store_dword v[6:7], v5, off offset:192
.LBB0_1532:
	s_or_b64 exec, exec, s[0:1]
	ds_read_b32 v5, v160 offset:108
	v_add_u32_e32 v4, 27, v4
	s_waitcnt lgkmcnt(0)
	v_rcp_f32_e32 v8, v5
	v_ashrrev_i32_e32 v5, 31, v4
	v_lshlrev_b64 v[6:7], 11, v[4:5]
	v_lshlrev_b64 v[4:5], 12, v[4:5]
	v_mul_f32_e32 v9, v81, v8
	s_nop 1
	v_mov_b32_dpp v11, v9 quad_perm:[1,0,3,2] row_mask:0xf bank_mask:0xf
	v_lshl_add_u64 v[6:7], s[6:7], 0, v[6:7]
	v_lshl_add_u64 v[4:5], s[8:9], 0, v[4:5]
	s_and_saveexec_b64 s[0:1], s[2:3]
	s_cbranch_execz .LBB0_1534
	v_lshl_add_u64 v[12:13], v[6:7], 0, v[2:3]
	global_load_dword v12, v[12:13], off
	s_waitcnt vmcnt(0)
	v_lshlrev_b32_e32 v13, 16, v12
	v_and_b32_e32 v12, 0xffff0000, v12
	v_mul_f32_e32 v9, v9, v13
	s_waitcnt lgkmcnt(0)
	v_mul_f32_e32 v11, v11, v12
	v_lshl_add_u64 v[12:13], v[4:5], 0, v[2:3]
	v_cvt_pk_bf16_f32 v9, v9, v11
	global_store_dword v[12:13], v9, off
.LBB0_1534:
	s_or_b64 exec, exec, s[0:1]
	v_mul_f32_e32 v9, v65, v8
	s_waitcnt lgkmcnt(0)
	s_nop 1
	v_mov_b32_dpp v11, v9 quad_perm:[1,0,3,2] row_mask:0xf bank_mask:0xf
	s_and_saveexec_b64 s[0:1], s[2:3]
	s_cbranch_execz .LBB0_1536
	v_lshl_add_u64 v[12:13], v[6:7], 0, v[2:3]
	global_load_dword v12, v[12:13], off offset:64
	s_waitcnt vmcnt(0)
	v_lshlrev_b32_e32 v13, 16, v12
	v_and_b32_e32 v12, 0xffff0000, v12
	v_mul_f32_e32 v9, v9, v13
	s_waitcnt lgkmcnt(0)
	v_mul_f32_e32 v11, v11, v12
	v_lshl_add_u64 v[12:13], v[4:5], 0, v[2:3]
	v_cvt_pk_bf16_f32 v9, v9, v11
	global_store_dword v[12:13], v9, off offset:64
.LBB0_1536:
	s_or_b64 exec, exec, s[0:1]
	v_mul_f32_e32 v9, v49, v8
	s_waitcnt lgkmcnt(0)
	s_nop 1
	v_mov_b32_dpp v11, v9 quad_perm:[1,0,3,2] row_mask:0xf bank_mask:0xf
	s_and_saveexec_b64 s[0:1], s[2:3]
	s_cbranch_execz .LBB0_1538
	v_lshl_add_u64 v[12:13], v[6:7], 0, v[2:3]
	global_load_dword v12, v[12:13], off offset:128
	s_waitcnt vmcnt(0)
	v_lshlrev_b32_e32 v13, 16, v12
	v_and_b32_e32 v12, 0xffff0000, v12
	v_mul_f32_e32 v9, v9, v13
	s_waitcnt lgkmcnt(0)
	v_mul_f32_e32 v11, v11, v12
	v_lshl_add_u64 v[12:13], v[4:5], 0, v[2:3]
	v_cvt_pk_bf16_f32 v9, v9, v11
	global_store_dword v[12:13], v9, off offset:128
.LBB0_1538:
	s_or_b64 exec, exec, s[0:1]
	v_mul_f32_e32 v8, v33, v8
	s_nop 1
	v_mov_b32_dpp v9, v8 quad_perm:[1,0,3,2] row_mask:0xf bank_mask:0xf
	s_and_saveexec_b64 s[0:1], s[2:3]
	s_xor_b64 s[0:1], exec, s[0:1]
	s_cbranch_execz .LBB0_1365
	v_lshl_add_u64 v[6:7], v[6:7], 0, v[2:3]
	global_load_dword v6, v[6:7], off offset:192
	v_lshl_add_u64 v[4:5], v[4:5], 0, v[2:3]
	s_waitcnt vmcnt(0)
	v_lshlrev_b32_e32 v7, 16, v6
	v_and_b32_e32 v6, 0xffff0000, v6
	s_waitcnt lgkmcnt(0)
	v_mul_f32_e32 v6, v9, v6
	v_mul_f32_e32 v7, v8, v7
	v_cvt_pk_bf16_f32 v6, v7, v6
	global_store_dword v[4:5], v6, off offset:192
	s_branch .LBB0_1365
